# weight-row int8 quantisation loops (3 instances in P1): next row's 8 loads prefetched into a separate register set right after the current row is unpacked; counted vmcnt
# baseline (speedup 1.0000x reference)
.LBB0_337:
	s_cmpk_gt_i32 s24, 0x33ff
	s_cbranch_scc1 .LBB0_342
	v_mbcnt_lo_u32_b32 v2, -1, 0
	v_mbcnt_hi_u32_b32 v2, -1, v2
	v_and_b32_e32 v3, 64, v2
	v_add_u32_e32 v3, 64, v3
	v_xor_b32_e32 v4, 1, v2
	v_cmp_lt_i32_e32 vcc, v4, v3
	s_ashr_i32 s25, s24, 31
	s_lshl_b64 s[0:1], s[24:25], 2
	v_cndmask_b32_e32 v4, v2, v4, vcc
	v_lshlrev_b32_e32 v6, 2, v4
	v_xor_b32_e32 v4, 2, v2
	v_cmp_lt_i32_e32 vcc, v4, v3
	s_add_u32 s10, s0, 0xca0000
	s_addc_u32 s11, s1, 0
	v_cndmask_b32_e32 v4, v2, v4, vcc
	v_lshlrev_b32_e32 v7, 2, v4
	v_xor_b32_e32 v4, 4, v2
	v_cmp_lt_i32_e32 vcc, v4, v3
	s_ashr_i32 s37, s36, 31
	s_lshl_b64 s[4:5], s[24:25], 12
	v_cndmask_b32_e32 v4, v2, v4, vcc
	v_lshlrev_b32_e32 v8, 2, v4
	v_xor_b32_e32 v4, 8, v2
	v_cmp_lt_i32_e32 vcc, v4, v3
	s_lshl_b64 s[6:7], s[24:25], 13
	v_cmp_eq_u32_e64 s[2:3], 0, v166
	v_cndmask_b32_e32 v4, v2, v4, vcc
	v_lshlrev_b32_e32 v9, 2, v4
	v_xor_b32_e32 v4, 16, v2
	v_cmp_lt_i32_e32 vcc, v4, v3
	s_lshl_b64 s[0:1], s[36:37], 2
	v_mov_b32_e32 v5, s7
	v_cndmask_b32_e32 v4, v2, v4, vcc
	v_lshlrev_b32_e32 v10, 2, v4
	v_xor_b32_e32 v4, 32, v2
	v_cmp_lt_i32_e32 vcc, v4, v3
	v_mov_b32_e32 v3, s5
	s_mov_b32 s12, 0x12a01000
	v_cndmask_b32_e32 v2, v2, v4, vcc
	v_lshlrev_b32_e32 v11, 2, v2
	v_lshl_or_b32 v2, v166, 3, s4
	s_lshl_b64 s[4:5], s[36:37], 12
	v_lshl_or_b32 v4, v166, 4, s6
	s_lshl_b64 s[6:7], s[36:37], 13
	s_mov_b32 s13, 0xda24260
	v_mov_b32_e32 v12, 0
	s_mov_b32 s25, 0x42fe0000
	s_mov_b32 s33, 0x4b3fff81
	s_mov_b32 s34, 0xc0c0400
	s_mov_b32 s35, 0x4000c0c
	s_mov_b32 s37, 0x53a00000
	v_mov_b32_e32 v13, 0x4b40007f
	s_mov_b32 s38, s24
	v_lshl_add_u64 v[120:121], s[68:69], 0, v[4:5]
	v_add_co_u32_e32 v136, vcc, s12, v120
	s_nop 1
	v_addc_co_u32_e32 v137, vcc, 0, v121, vcc
	v_add_co_u32_e32 v144, vcc, 0x12a00000, v120
	global_load_dwordx4 v[102:105], v[136:137], off
	global_load_dwordx4 v[106:109], v[136:137], off offset:1024
	global_load_dwordx4 v[110:113], v[136:137], off offset:2048
	s_nop 0
	global_load_dwordx4 v[116:119], v[136:137], off offset:3072
	v_addc_co_u32_e32 v145, vcc, 0, v121, vcc
	global_load_dwordx4 v[128:131], v[144:145], off
	global_load_dwordx4 v[132:135], v[144:145], off offset:1024
	global_load_dwordx4 v[168:171], v[144:145], off offset:2048
	s_nop 0
	global_load_dwordx4 v[172:175], v[144:145], off offset:3072
	s_waitcnt vmcnt(7)
	v_cvt_f32_f16_e32 v46, v102
	v_cvt_f32_f16_sdwa v14, v102 dst_sel:DWORD dst_unused:UNUSED_PAD src0_sel:WORD_1
	v_cvt_f32_f16_e32 v47, v103
	v_cvt_f32_f16_sdwa v15, v103 dst_sel:DWORD dst_unused:UNUSED_PAD src0_sel:WORD_1
	v_cvt_f32_f16_e32 v48, v104
	v_cvt_f32_f16_sdwa v16, v104 dst_sel:DWORD dst_unused:UNUSED_PAD src0_sel:WORD_1
	v_cvt_f32_f16_e32 v49, v105
	v_cvt_f32_f16_sdwa v17, v105 dst_sel:DWORD dst_unused:UNUSED_PAD src0_sel:WORD_1
	s_waitcnt vmcnt(6)
	v_cvt_f32_f16_e32 v50, v106
	v_cvt_f32_f16_sdwa v18, v106 dst_sel:DWORD dst_unused:UNUSED_PAD src0_sel:WORD_1
	v_cvt_f32_f16_e32 v51, v107
	v_cvt_f32_f16_sdwa v19, v107 dst_sel:DWORD dst_unused:UNUSED_PAD src0_sel:WORD_1
	v_cvt_f32_f16_e32 v52, v108
	v_cvt_f32_f16_sdwa v20, v108 dst_sel:DWORD dst_unused:UNUSED_PAD src0_sel:WORD_1
	v_cvt_f32_f16_e32 v53, v109
	v_cvt_f32_f16_sdwa v21, v109 dst_sel:DWORD dst_unused:UNUSED_PAD src0_sel:WORD_1
	s_waitcnt vmcnt(5)
	v_cvt_f32_f16_e32 v54, v110
	v_cvt_f32_f16_sdwa v22, v110 dst_sel:DWORD dst_unused:UNUSED_PAD src0_sel:WORD_1
	v_cvt_f32_f16_e32 v55, v111
	v_cvt_f32_f16_sdwa v23, v111 dst_sel:DWORD dst_unused:UNUSED_PAD src0_sel:WORD_1
	v_cvt_f32_f16_e32 v56, v112
	v_cvt_f32_f16_sdwa v24, v112 dst_sel:DWORD dst_unused:UNUSED_PAD src0_sel:WORD_1
	v_cvt_f32_f16_e32 v57, v113
	v_cvt_f32_f16_sdwa v25, v113 dst_sel:DWORD dst_unused:UNUSED_PAD src0_sel:WORD_1
	s_waitcnt vmcnt(4)
	v_cvt_f32_f16_e32 v58, v116
	v_cvt_f32_f16_sdwa v26, v116 dst_sel:DWORD dst_unused:UNUSED_PAD src0_sel:WORD_1
	v_cvt_f32_f16_e32 v59, v117
	v_cvt_f32_f16_sdwa v27, v117 dst_sel:DWORD dst_unused:UNUSED_PAD src0_sel:WORD_1
	v_cvt_f32_f16_e32 v60, v118
	v_cvt_f32_f16_sdwa v28, v118 dst_sel:DWORD dst_unused:UNUSED_PAD src0_sel:WORD_1
	v_cvt_f32_f16_e32 v61, v119
	v_cvt_f32_f16_sdwa v29, v119 dst_sel:DWORD dst_unused:UNUSED_PAD src0_sel:WORD_1
	s_waitcnt vmcnt(3)
	v_cvt_f32_f16_e32 v62, v128
	v_cvt_f32_f16_sdwa v30, v128 dst_sel:DWORD dst_unused:UNUSED_PAD src0_sel:WORD_1
	v_cvt_f32_f16_e32 v63, v129
	v_cvt_f32_f16_sdwa v31, v129 dst_sel:DWORD dst_unused:UNUSED_PAD src0_sel:WORD_1
	v_cvt_f32_f16_e32 v64, v130
	v_cvt_f32_f16_sdwa v32, v130 dst_sel:DWORD dst_unused:UNUSED_PAD src0_sel:WORD_1
	v_cvt_f32_f16_e32 v65, v131
	v_cvt_f32_f16_sdwa v33, v131 dst_sel:DWORD dst_unused:UNUSED_PAD src0_sel:WORD_1
	s_waitcnt vmcnt(2)
	v_cvt_f32_f16_e32 v66, v132
	v_cvt_f32_f16_sdwa v34, v132 dst_sel:DWORD dst_unused:UNUSED_PAD src0_sel:WORD_1
	v_cvt_f32_f16_e32 v67, v133
	v_cvt_f32_f16_sdwa v35, v133 dst_sel:DWORD dst_unused:UNUSED_PAD src0_sel:WORD_1
	v_cvt_f32_f16_e32 v68, v134
	v_cvt_f32_f16_sdwa v36, v134 dst_sel:DWORD dst_unused:UNUSED_PAD src0_sel:WORD_1
	v_cvt_f32_f16_e32 v69, v135
	v_cvt_f32_f16_sdwa v37, v135 dst_sel:DWORD dst_unused:UNUSED_PAD src0_sel:WORD_1
	s_waitcnt vmcnt(1)
	v_cvt_f32_f16_e32 v70, v168
	v_cvt_f32_f16_sdwa v38, v168 dst_sel:DWORD dst_unused:UNUSED_PAD src0_sel:WORD_1
	v_cvt_f32_f16_e32 v71, v169
	v_cvt_f32_f16_sdwa v39, v169 dst_sel:DWORD dst_unused:UNUSED_PAD src0_sel:WORD_1
	v_cvt_f32_f16_e32 v72, v170
	v_cvt_f32_f16_sdwa v40, v170 dst_sel:DWORD dst_unused:UNUSED_PAD src0_sel:WORD_1
	v_cvt_f32_f16_e32 v73, v171
	v_cvt_f32_f16_sdwa v41, v171 dst_sel:DWORD dst_unused:UNUSED_PAD src0_sel:WORD_1
	s_waitcnt vmcnt(0)
	v_cvt_f32_f16_e32 v74, v172
	v_cvt_f32_f16_sdwa v42, v172 dst_sel:DWORD dst_unused:UNUSED_PAD src0_sel:WORD_1
	v_cvt_f32_f16_e32 v75, v173
	v_cvt_f32_f16_sdwa v43, v173 dst_sel:DWORD dst_unused:UNUSED_PAD src0_sel:WORD_1
	v_cvt_f32_f16_e32 v76, v174
	v_cvt_f32_f16_sdwa v44, v174 dst_sel:DWORD dst_unused:UNUSED_PAD src0_sel:WORD_1
	v_cvt_f32_f16_e32 v77, v175
	v_cvt_f32_f16_sdwa v45, v175 dst_sel:DWORD dst_unused:UNUSED_PAD src0_sel:WORD_1
	s_branch .Lrp_q1_go

.LBB0_340:
	s_waitcnt vmcnt(16)
	v_cvt_f32_f16_e32 v46, v102
	v_cvt_f32_f16_sdwa v14, v102 dst_sel:DWORD dst_unused:UNUSED_PAD src0_sel:WORD_1
	v_cvt_f32_f16_e32 v47, v103
	v_cvt_f32_f16_sdwa v15, v103 dst_sel:DWORD dst_unused:UNUSED_PAD src0_sel:WORD_1
	v_cvt_f32_f16_e32 v48, v104
	v_cvt_f32_f16_sdwa v16, v104 dst_sel:DWORD dst_unused:UNUSED_PAD src0_sel:WORD_1
	v_cvt_f32_f16_e32 v49, v105
	v_cvt_f32_f16_sdwa v17, v105 dst_sel:DWORD dst_unused:UNUSED_PAD src0_sel:WORD_1
	s_waitcnt vmcnt(15)
	v_cvt_f32_f16_e32 v50, v106
	v_cvt_f32_f16_sdwa v18, v106 dst_sel:DWORD dst_unused:UNUSED_PAD src0_sel:WORD_1
	v_cvt_f32_f16_e32 v51, v107
	v_cvt_f32_f16_sdwa v19, v107 dst_sel:DWORD dst_unused:UNUSED_PAD src0_sel:WORD_1
	v_cvt_f32_f16_e32 v52, v108
	v_cvt_f32_f16_sdwa v20, v108 dst_sel:DWORD dst_unused:UNUSED_PAD src0_sel:WORD_1
	v_cvt_f32_f16_e32 v53, v109
	v_cvt_f32_f16_sdwa v21, v109 dst_sel:DWORD dst_unused:UNUSED_PAD src0_sel:WORD_1
	s_waitcnt vmcnt(14)
	v_cvt_f32_f16_e32 v54, v110
	v_cvt_f32_f16_sdwa v22, v110 dst_sel:DWORD dst_unused:UNUSED_PAD src0_sel:WORD_1
	v_cvt_f32_f16_e32 v55, v111
	v_cvt_f32_f16_sdwa v23, v111 dst_sel:DWORD dst_unused:UNUSED_PAD src0_sel:WORD_1
	v_cvt_f32_f16_e32 v56, v112
	v_cvt_f32_f16_sdwa v24, v112 dst_sel:DWORD dst_unused:UNUSED_PAD src0_sel:WORD_1
	v_cvt_f32_f16_e32 v57, v113
	v_cvt_f32_f16_sdwa v25, v113 dst_sel:DWORD dst_unused:UNUSED_PAD src0_sel:WORD_1
	s_waitcnt vmcnt(13)
	v_cvt_f32_f16_e32 v58, v116
	v_cvt_f32_f16_sdwa v26, v116 dst_sel:DWORD dst_unused:UNUSED_PAD src0_sel:WORD_1
	v_cvt_f32_f16_e32 v59, v117
	v_cvt_f32_f16_sdwa v27, v117 dst_sel:DWORD dst_unused:UNUSED_PAD src0_sel:WORD_1
	v_cvt_f32_f16_e32 v60, v118
	v_cvt_f32_f16_sdwa v28, v118 dst_sel:DWORD dst_unused:UNUSED_PAD src0_sel:WORD_1
	v_cvt_f32_f16_e32 v61, v119
	v_cvt_f32_f16_sdwa v29, v119 dst_sel:DWORD dst_unused:UNUSED_PAD src0_sel:WORD_1
	s_waitcnt vmcnt(12)
	v_cvt_f32_f16_e32 v62, v128
	v_cvt_f32_f16_sdwa v30, v128 dst_sel:DWORD dst_unused:UNUSED_PAD src0_sel:WORD_1
	v_cvt_f32_f16_e32 v63, v129
	v_cvt_f32_f16_sdwa v31, v129 dst_sel:DWORD dst_unused:UNUSED_PAD src0_sel:WORD_1
	v_cvt_f32_f16_e32 v64, v130
	v_cvt_f32_f16_sdwa v32, v130 dst_sel:DWORD dst_unused:UNUSED_PAD src0_sel:WORD_1
	v_cvt_f32_f16_e32 v65, v131
	v_cvt_f32_f16_sdwa v33, v131 dst_sel:DWORD dst_unused:UNUSED_PAD src0_sel:WORD_1
	s_waitcnt vmcnt(11)
	v_cvt_f32_f16_e32 v66, v132
	v_cvt_f32_f16_sdwa v34, v132 dst_sel:DWORD dst_unused:UNUSED_PAD src0_sel:WORD_1
	v_cvt_f32_f16_e32 v67, v133
	v_cvt_f32_f16_sdwa v35, v133 dst_sel:DWORD dst_unused:UNUSED_PAD src0_sel:WORD_1
	v_cvt_f32_f16_e32 v68, v134
	v_cvt_f32_f16_sdwa v36, v134 dst_sel:DWORD dst_unused:UNUSED_PAD src0_sel:WORD_1
	v_cvt_f32_f16_e32 v69, v135
	v_cvt_f32_f16_sdwa v37, v135 dst_sel:DWORD dst_unused:UNUSED_PAD src0_sel:WORD_1
	s_waitcnt vmcnt(10)
	v_cvt_f32_f16_e32 v70, v168
	v_cvt_f32_f16_sdwa v38, v168 dst_sel:DWORD dst_unused:UNUSED_PAD src0_sel:WORD_1
	v_cvt_f32_f16_e32 v71, v169
	v_cvt_f32_f16_sdwa v39, v169 dst_sel:DWORD dst_unused:UNUSED_PAD src0_sel:WORD_1
	v_cvt_f32_f16_e32 v72, v170
	v_cvt_f32_f16_sdwa v40, v170 dst_sel:DWORD dst_unused:UNUSED_PAD src0_sel:WORD_1
	v_cvt_f32_f16_e32 v73, v171
	v_cvt_f32_f16_sdwa v41, v171 dst_sel:DWORD dst_unused:UNUSED_PAD src0_sel:WORD_1
	s_waitcnt vmcnt(9)
	v_cvt_f32_f16_e32 v74, v172
	v_cvt_f32_f16_sdwa v42, v172 dst_sel:DWORD dst_unused:UNUSED_PAD src0_sel:WORD_1
	v_cvt_f32_f16_e32 v75, v173
	v_cvt_f32_f16_sdwa v43, v173 dst_sel:DWORD dst_unused:UNUSED_PAD src0_sel:WORD_1
	v_cvt_f32_f16_e32 v76, v174
	v_cvt_f32_f16_sdwa v44, v174 dst_sel:DWORD dst_unused:UNUSED_PAD src0_sel:WORD_1
	v_cvt_f32_f16_e32 v77, v175
	v_cvt_f32_f16_sdwa v45, v175 dst_sel:DWORD dst_unused:UNUSED_PAD src0_sel:WORD_1
.Lrp_q1_go:
	v_lshl_add_u64 v[120:121], v[4:5], 0, s[6:7]
	v_lshl_add_u64 v[120:121], s[68:69], 0, v[120:121]
	v_add_co_u32_e32 v136, vcc, s12, v120
	s_nop 1
	v_addc_co_u32_e32 v137, vcc, 0, v121, vcc
	v_add_co_u32_e32 v144, vcc, 0x12a00000, v120
	global_load_dwordx4 v[102:105], v[136:137], off
	global_load_dwordx4 v[106:109], v[136:137], off offset:1024
	global_load_dwordx4 v[110:113], v[136:137], off offset:2048
	s_nop 0
	global_load_dwordx4 v[116:119], v[136:137], off offset:3072
	v_addc_co_u32_e32 v145, vcc, 0, v121, vcc
	global_load_dwordx4 v[128:131], v[144:145], off
	global_load_dwordx4 v[132:135], v[144:145], off offset:1024
	global_load_dwordx4 v[168:171], v[144:145], off offset:2048
	s_nop 0
	global_load_dwordx4 v[172:175], v[144:145], off offset:3072
	v_add_f32_e32 v78, v62, v30
	v_sub_f32_e32 v30, v62, v30
	v_add_f32_e32 v62, v63, v31
	v_sub_f32_e32 v31, v63, v31
	v_add_f32_e32 v63, v64, v32
	v_sub_f32_e32 v32, v64, v32
	v_add_f32_e32 v64, v65, v33
	v_sub_f32_e32 v33, v65, v33
	v_add_f32_e32 v65, v66, v34
	v_sub_f32_e32 v34, v66, v34
	v_add_f32_e32 v66, v67, v35
	v_sub_f32_e32 v35, v67, v35
	v_add_f32_e32 v67, v68, v36
	v_sub_f32_e32 v36, v68, v36
	v_add_f32_e32 v68, v69, v37
	v_sub_f32_e32 v37, v69, v37
	v_add_f32_e32 v69, v70, v38
	v_sub_f32_e32 v38, v70, v38
	v_add_f32_e32 v70, v71, v39
	v_sub_f32_e32 v39, v71, v39
	v_add_f32_e32 v71, v72, v40
	v_sub_f32_e32 v40, v72, v40
	v_add_f32_e32 v72, v73, v41
	v_sub_f32_e32 v41, v73, v41
	v_add_f32_e32 v73, v74, v42
	v_sub_f32_e32 v42, v74, v42
	v_add_f32_e32 v74, v75, v43
	v_sub_f32_e32 v43, v75, v43
	v_add_f32_e32 v75, v76, v44
	v_sub_f32_e32 v44, v76, v44
	v_add_f32_e32 v76, v77, v45
	v_sub_f32_e32 v45, v77, v45
	v_add_f32_e32 v77, v46, v14
	v_sub_f32_e32 v14, v46, v14
	v_add_f32_e32 v46, v47, v15
	v_sub_f32_e32 v15, v47, v15
	v_add_f32_e32 v47, v48, v16
	v_sub_f32_e32 v16, v48, v16
	v_add_f32_e32 v48, v49, v17
	v_sub_f32_e32 v17, v49, v17
	v_add_f32_e32 v49, v50, v18
	v_sub_f32_e32 v18, v50, v18
	v_add_f32_e32 v50, v51, v19
	v_sub_f32_e32 v19, v51, v19
	v_add_f32_e32 v51, v52, v20
	v_sub_f32_e32 v20, v52, v20
	v_add_f32_e32 v52, v53, v21
	v_sub_f32_e32 v21, v53, v21
	v_add_f32_e32 v53, v54, v22
	v_sub_f32_e32 v22, v54, v22
	v_add_f32_e32 v54, v55, v23
	v_sub_f32_e32 v23, v55, v23
	v_add_f32_e32 v55, v56, v24
	v_sub_f32_e32 v24, v56, v24
	v_add_f32_e32 v56, v57, v25
	v_sub_f32_e32 v25, v57, v25
	v_add_f32_e32 v57, v58, v26
	v_sub_f32_e32 v26, v58, v26
	v_add_f32_e32 v58, v59, v27
	v_sub_f32_e32 v27, v59, v27
	v_add_f32_e32 v59, v60, v28
	v_sub_f32_e32 v28, v60, v28
	v_add_f32_e32 v60, v61, v29
	v_sub_f32_e32 v29, v61, v29
	v_add_f32_e32 v61, v78, v62
	v_sub_f32_e32 v62, v78, v62
	v_add_f32_e32 v78, v30, v31
	v_sub_f32_e32 v30, v30, v31
	v_add_f32_e32 v31, v63, v64
	v_sub_f32_e32 v63, v63, v64
	v_add_f32_e32 v64, v32, v33
	v_sub_f32_e32 v32, v32, v33
	v_add_f32_e32 v33, v65, v66
	v_sub_f32_e32 v65, v65, v66
	v_add_f32_e32 v66, v34, v35
	v_sub_f32_e32 v34, v34, v35
	v_add_f32_e32 v35, v67, v68
	v_sub_f32_e32 v67, v67, v68
	v_add_f32_e32 v68, v36, v37
	v_sub_f32_e32 v36, v36, v37
	v_add_f32_e32 v37, v69, v70
	v_sub_f32_e32 v69, v69, v70
	v_add_f32_e32 v70, v38, v39
	v_sub_f32_e32 v38, v38, v39
	v_add_f32_e32 v39, v71, v72
	v_sub_f32_e32 v71, v71, v72
	v_add_f32_e32 v72, v40, v41
	v_sub_f32_e32 v40, v40, v41
	v_add_f32_e32 v41, v73, v74
	v_sub_f32_e32 v73, v73, v74
	v_add_f32_e32 v74, v42, v43
	v_sub_f32_e32 v42, v42, v43
	v_add_f32_e32 v43, v75, v76
	v_sub_f32_e32 v75, v75, v76
	v_add_f32_e32 v76, v44, v45
	v_sub_f32_e32 v44, v44, v45
	v_add_f32_e32 v45, v77, v46
	v_sub_f32_e32 v46, v77, v46
	v_add_f32_e32 v77, v14, v15
	v_sub_f32_e32 v14, v14, v15
	v_add_f32_e32 v15, v47, v48
	v_sub_f32_e32 v47, v47, v48
	v_add_f32_e32 v48, v16, v17
	v_sub_f32_e32 v16, v16, v17
	v_add_f32_e32 v17, v49, v50
	v_sub_f32_e32 v49, v49, v50
	v_add_f32_e32 v50, v18, v19
	v_sub_f32_e32 v18, v18, v19
	v_add_f32_e32 v19, v51, v52
	v_sub_f32_e32 v51, v51, v52
	v_add_f32_e32 v52, v20, v21
	v_sub_f32_e32 v20, v20, v21
	v_add_f32_e32 v21, v53, v54
	v_sub_f32_e32 v53, v53, v54
	v_add_f32_e32 v54, v22, v23
	v_sub_f32_e32 v22, v22, v23
	v_add_f32_e32 v23, v55, v56
	v_sub_f32_e32 v55, v55, v56
	v_add_f32_e32 v56, v24, v25
	v_sub_f32_e32 v24, v24, v25
	v_add_f32_e32 v25, v57, v58
	v_sub_f32_e32 v57, v57, v58
	v_add_f32_e32 v58, v26, v27
	v_sub_f32_e32 v26, v26, v27
	v_add_f32_e32 v27, v59, v60
	v_sub_f32_e32 v59, v59, v60
	v_add_f32_e32 v60, v28, v29
	v_sub_f32_e32 v28, v28, v29
	v_add_f32_e32 v29, v61, v31
	v_sub_f32_e32 v31, v61, v31
	v_add_f32_e32 v61, v78, v64
	v_sub_f32_e32 v64, v78, v64
	v_add_f32_e32 v78, v62, v63
	v_sub_f32_e32 v62, v62, v63
	v_add_f32_e32 v63, v30, v32
	v_sub_f32_e32 v30, v30, v32
	v_add_f32_e32 v32, v33, v35
	v_sub_f32_e32 v33, v33, v35
	v_add_f32_e32 v35, v66, v68
	v_sub_f32_e32 v66, v66, v68
	v_add_f32_e32 v68, v65, v67
	v_sub_f32_e32 v65, v65, v67
	v_add_f32_e32 v67, v34, v36
	v_sub_f32_e32 v34, v34, v36
	v_add_f32_e32 v36, v37, v39
	v_sub_f32_e32 v37, v37, v39
	v_add_f32_e32 v39, v70, v72
	v_sub_f32_e32 v70, v70, v72
	v_add_f32_e32 v72, v69, v71
	v_sub_f32_e32 v69, v69, v71
	v_add_f32_e32 v71, v38, v40
	v_sub_f32_e32 v38, v38, v40
	v_add_f32_e32 v40, v41, v43
	v_sub_f32_e32 v41, v41, v43
	v_add_f32_e32 v43, v74, v76
	v_sub_f32_e32 v74, v74, v76
	v_add_f32_e32 v76, v73, v75
	v_sub_f32_e32 v73, v73, v75
	v_add_f32_e32 v75, v42, v44
	v_sub_f32_e32 v42, v42, v44
	v_add_f32_e32 v44, v45, v15
	v_sub_f32_e32 v15, v45, v15
	v_add_f32_e32 v45, v77, v48
	v_sub_f32_e32 v48, v77, v48
	v_add_f32_e32 v77, v46, v47
	v_sub_f32_e32 v46, v46, v47
	v_add_f32_e32 v47, v14, v16
	v_sub_f32_e32 v14, v14, v16
	v_add_f32_e32 v16, v17, v19
	v_sub_f32_e32 v17, v17, v19
	v_add_f32_e32 v19, v50, v52
	v_sub_f32_e32 v50, v50, v52
	v_add_f32_e32 v52, v49, v51
	v_sub_f32_e32 v49, v49, v51
	v_add_f32_e32 v51, v18, v20
	v_sub_f32_e32 v18, v18, v20
	v_add_f32_e32 v20, v21, v23
	v_sub_f32_e32 v21, v21, v23
	v_add_f32_e32 v23, v54, v56
	v_sub_f32_e32 v54, v54, v56
	v_add_f32_e32 v56, v53, v55
	v_sub_f32_e32 v53, v53, v55
	v_add_f32_e32 v55, v22, v24
	v_sub_f32_e32 v22, v22, v24
	v_add_f32_e32 v24, v25, v27
	v_sub_f32_e32 v25, v25, v27
	v_add_f32_e32 v27, v58, v60
	v_sub_f32_e32 v58, v58, v60
	v_add_f32_e32 v60, v57, v59
	v_sub_f32_e32 v57, v57, v59
	v_add_f32_e32 v59, v26, v28
	v_sub_f32_e32 v26, v26, v28
	v_add_f32_e32 v28, v29, v32
	v_sub_f32_e32 v29, v29, v32
	v_add_f32_e32 v32, v61, v35
	v_sub_f32_e32 v35, v61, v35
	v_add_f32_e32 v61, v78, v68
	v_sub_f32_e32 v68, v78, v68
	v_add_f32_e32 v78, v63, v67
	v_sub_f32_e32 v63, v63, v67
	v_add_f32_e32 v67, v31, v33
	v_sub_f32_e32 v31, v31, v33
	v_add_f32_e32 v33, v64, v66
	v_sub_f32_e32 v64, v64, v66
	v_add_f32_e32 v66, v62, v65
	v_sub_f32_e32 v62, v62, v65
	v_add_f32_e32 v65, v30, v34
	v_sub_f32_e32 v30, v30, v34
	v_add_f32_e32 v34, v36, v40
	v_sub_f32_e32 v36, v36, v40
	v_add_f32_e32 v40, v39, v43
	v_sub_f32_e32 v39, v39, v43
	v_add_f32_e32 v43, v72, v76
	v_sub_f32_e32 v72, v72, v76
	v_add_f32_e32 v76, v71, v75
	v_sub_f32_e32 v71, v71, v75
	v_add_f32_e32 v75, v37, v41
	v_sub_f32_e32 v37, v37, v41
	v_add_f32_e32 v41, v70, v74
	v_sub_f32_e32 v70, v70, v74
	v_add_f32_e32 v74, v69, v73
	v_sub_f32_e32 v69, v69, v73
	v_add_f32_e32 v73, v38, v42
	v_sub_f32_e32 v38, v38, v42
	v_add_f32_e32 v42, v44, v16
	v_sub_f32_e32 v16, v44, v16
	v_add_f32_e32 v44, v45, v19
	v_sub_f32_e32 v19, v45, v19
	v_add_f32_e32 v45, v77, v52
	v_sub_f32_e32 v52, v77, v52
	v_add_f32_e32 v77, v47, v51
	v_sub_f32_e32 v47, v47, v51
	v_add_f32_e32 v51, v15, v17
	v_sub_f32_e32 v15, v15, v17
	v_add_f32_e32 v17, v48, v50
	v_sub_f32_e32 v48, v48, v50
	v_add_f32_e32 v50, v46, v49
	v_sub_f32_e32 v46, v46, v49
	v_add_f32_e32 v49, v14, v18
	v_sub_f32_e32 v14, v14, v18
	v_add_f32_e32 v18, v20, v24
	v_sub_f32_e32 v20, v20, v24
	v_add_f32_e32 v24, v23, v27
	v_sub_f32_e32 v23, v23, v27
	v_add_f32_e32 v27, v56, v60
	v_sub_f32_e32 v56, v56, v60
	v_add_f32_e32 v60, v55, v59
	v_sub_f32_e32 v55, v55, v59
	v_add_f32_e32 v59, v21, v25
	v_sub_f32_e32 v21, v21, v25
	v_add_f32_e32 v25, v54, v58
	v_sub_f32_e32 v54, v54, v58
	v_add_f32_e32 v58, v53, v57
	v_sub_f32_e32 v53, v53, v57
	v_add_f32_e32 v57, v22, v26
	v_sub_f32_e32 v22, v22, v26
	v_add_f32_e32 v26, v28, v34
	v_sub_f32_e32 v28, v28, v34
	v_add_f32_e32 v34, v32, v40
	v_add_f32_e32 v80, v67, v75
	v_sub_f32_e32 v81, v67, v75
	v_add_f32_e32 v67, v33, v41
	v_sub_f32_e32 v82, v33, v41
	v_add_f32_e32 v41, v65, v73
	v_sub_f32_e32 v84, v65, v73
	v_add_f32_e32 v65, v29, v36
	v_sub_f32_e32 v85, v29, v36
	v_add_f32_e32 v29, v35, v39
	v_sub_f32_e32 v86, v35, v39
	v_add_f32_e32 v94, v30, v38
	v_sub_f32_e32 v95, v30, v38
	v_add_f32_e32 v30, v42, v18
	v_add_f32_e32 v35, v44, v24
	v_sub_f32_e32 v79, v32, v40
	v_add_f32_e32 v32, v61, v43
	v_sub_f32_e32 v61, v61, v43
	v_add_f32_e32 v40, v78, v76
	v_sub_f32_e32 v78, v78, v76
	v_add_f32_e32 v33, v66, v74
	v_sub_f32_e32 v83, v66, v74
	v_add_f32_e32 v88, v63, v71
	v_sub_f32_e32 v89, v63, v71
	v_add_f32_e32 v63, v31, v37
	v_sub_f32_e32 v90, v31, v37
	v_sub_f32_e32 v18, v42, v18
	v_add_f32_e32 v37, v45, v27
	v_sub_f32_e32 v96, v45, v27
	v_add_f32_e32 v27, v77, v60
	v_sub_f32_e32 v97, v77, v60
	v_add_f32_e32 v39, v17, v25
	v_sub_f32_e32 v17, v17, v25
	v_add_f32_e32 v25, v50, v58
	v_sub_f32_e32 v50, v50, v58
	v_add_f32_e32 v58, v49, v57
	v_sub_f32_e32 v49, v49, v57
	v_add_f32_e32 v57, v16, v20
	v_sub_f32_e32 v16, v16, v20
	v_add_f32_e32 v20, v19, v23
	v_add_f32_e32 v74, v26, v30
	v_add_f32_e32 v75, v34, v35
	v_add_f32_e32 v38, v51, v59
	v_sub_f32_e32 v42, v26, v30
	v_sub_f32_e32 v43, v34, v35
	v_add_f32_e32 v76, v32, v37
	v_add_f32_e32 v77, v40, v27
	v_add_f32_e32 v71, v67, v39
	v_sub_f32_e32 v39, v67, v39
	v_add_f32_e32 v73, v41, v58
	v_sub_f32_e32 v41, v41, v58
	v_add_f32_e32 v67, v29, v20
	v_sub_f32_e32 v35, v29, v20
	v_add_f32_e32 v58, v28, v18
	v_sub_f32_e32 v26, v28, v18
	v_add_f32_e32 v60, v61, v96
	v_sub_f32_e32 v28, v61, v96
	v_add_f32_e32 v61, v78, v97
	v_sub_f32_e32 v29, v78, v97
	v_max3_f32 v78, |v74|, 0, |v75|
	v_add_f32_e32 v31, v64, v70
	v_sub_f32_e32 v91, v64, v70
	v_add_f32_e32 v70, v80, v38
	v_max3_f32 v78, v78, |v76|, |v77|
	v_add_f32_e32 v36, v68, v72
	v_sub_f32_e32 v87, v68, v72
	v_add_f32_e32 v72, v33, v25
	v_max3_f32 v78, v78, |v70|, |v71|
	v_sub_f32_e32 v19, v19, v23
	v_add_f32_e32 v23, v52, v56
	v_sub_f32_e32 v98, v52, v56
	v_add_f32_e32 v52, v47, v55
	v_add_f32_e32 v66, v65, v57
	v_max3_f32 v78, v78, |v72|, |v73|
	v_add_f32_e32 v92, v62, v69
	v_sub_f32_e32 v93, v62, v69
	v_sub_f32_e32 v47, v47, v55
	v_add_f32_e32 v55, v15, v21
	v_sub_f32_e32 v15, v15, v21
	v_add_f32_e32 v21, v48, v54
	v_add_f32_e32 v68, v36, v23
	v_add_f32_e32 v69, v88, v52
	v_max3_f32 v78, v78, |v66|, |v67|
	v_sub_f32_e32 v48, v48, v54
	v_add_f32_e32 v54, v46, v53
	v_sub_f32_e32 v99, v46, v53
	v_add_f32_e32 v46, v14, v22
	v_add_f32_e32 v62, v63, v55
	v_sub_f32_e32 v30, v63, v55
	v_add_f32_e32 v63, v31, v21
	v_max3_f32 v78, v78, |v68|, |v69|
	v_sub_f32_e32 v24, v44, v24
	v_sub_f32_e32 v34, v65, v57
	v_add_f32_e32 v64, v92, v54
	v_add_f32_e32 v65, v94, v46
	v_max3_f32 v78, v78, |v62|, |v63|
	v_sub_f32_e32 v51, v51, v59
	v_add_f32_e32 v59, v79, v24
	v_max3_f32 v78, v78, |v64|, |v65|
	v_max3_f32 v78, v78, |v58|, |v59|
	v_sub_f32_e32 v44, v32, v37
	v_sub_f32_e32 v32, v92, v54
	v_add_f32_e32 v54, v81, v51
	v_add_f32_e32 v55, v82, v17
	v_max3_f32 v78, v78, |v60|, |v61|
	v_add_f32_e32 v56, v83, v50
	v_add_f32_e32 v57, v84, v49
	v_max3_f32 v78, v78, |v54|, |v55|
	v_sub_f32_e32 v100, v14, v22
	v_sub_f32_e32 v45, v40, v27
	v_sub_f32_e32 v27, v79, v24
	v_sub_f32_e32 v22, v81, v51
	v_sub_f32_e32 v24, v83, v50
	v_add_f32_e32 v50, v85, v16
	v_add_f32_e32 v51, v86, v19
	v_max3_f32 v78, v78, |v56|, |v57|
	v_sub_f32_e32 v37, v88, v52
	v_add_f32_e32 v52, v87, v98
	v_add_f32_e32 v53, v89, v47
	v_max3_f32 v78, v78, |v50|, |v51|
	v_sub_f32_e32 v40, v33, v25
	v_sub_f32_e32 v31, v31, v21
	v_sub_f32_e32 v33, v94, v46
	v_sub_f32_e32 v21, v89, v47
	v_add_f32_e32 v46, v90, v15
	v_add_f32_e32 v47, v91, v48
	v_max3_f32 v78, v78, |v52|, |v53|
	v_sub_f32_e32 v25, v84, v49
	v_sub_f32_e32 v14, v90, v15
	v_sub_f32_e32 v15, v91, v48
	v_add_f32_e32 v48, v93, v99
	v_add_f32_e32 v49, v95, v100
	v_max3_f32 v78, v78, |v46|, |v47|
	v_max3_f32 v78, v78, |v48|, |v49|
	v_max3_f32 v78, v78, |v42|, |v43|
	v_sub_f32_e32 v38, v80, v38
	v_max3_f32 v78, v78, |v44|, |v45|
	v_max3_f32 v78, v78, |v38|, |v39|
	v_max3_f32 v78, v78, |v40|, |v41|
	v_sub_f32_e32 v36, v36, v23
	v_max3_f32 v78, v78, |v34|, |v35|
	v_max3_f32 v78, v78, |v36|, |v37|
	v_max3_f32 v78, v78, |v30|, |v31|
	v_max3_f32 v78, v78, |v32|, |v33|
	v_max3_f32 v78, v78, |v26|, |v27|
	v_sub_f32_e32 v23, v82, v17
	v_max3_f32 v78, v78, |v28|, |v29|
	v_max3_f32 v78, v78, |v22|, |v23|
	v_sub_f32_e32 v18, v85, v16
	v_sub_f32_e32 v19, v86, v19
	v_max3_f32 v78, v78, |v24|, |v25|
	v_sub_f32_e32 v20, v87, v98
	v_max3_f32 v78, v78, |v18|, |v19|
	v_max3_f32 v78, v78, |v20|, |v21|
	v_sub_f32_e32 v16, v93, v99
	v_sub_f32_e32 v17, v95, v100
	v_max3_f32 v78, v78, |v14|, |v15|
	v_max3_f32 v78, v78, |v16|, |v17|
	ds_bpermute_b32 v79, v6, v78
	s_waitcnt lgkmcnt(0)
	v_max_f32_e32 v79, v79, v79
	v_max_f32_e32 v78, v78, v79
	ds_bpermute_b32 v79, v7, v78
	s_waitcnt lgkmcnt(0)
	v_max_f32_e32 v79, v79, v79
	v_max_f32_e32 v78, v78, v79
	ds_bpermute_b32 v79, v8, v78
	s_waitcnt lgkmcnt(0)
	v_max_f32_e32 v79, v79, v79
	v_max_f32_e32 v78, v78, v79
	ds_bpermute_b32 v79, v9, v78
	s_waitcnt lgkmcnt(0)
	v_max_f32_e32 v79, v79, v79
	v_max_f32_e32 v78, v78, v79
	ds_bpermute_b32 v79, v10, v78
	s_waitcnt lgkmcnt(0)
	v_max_f32_e32 v79, v79, v79
	v_max_f32_e32 v78, v78, v79
	ds_bpermute_b32 v79, v11, v78
	s_waitcnt lgkmcnt(0)
	v_max3_f32 v78, v78, v79, s13
	s_and_saveexec_b64 s[8:9], s[2:3]
	s_cbranch_execz .LBB0_339
	s_add_u32 s40, s68, s10
	s_addc_u32 s41, s69, s11
	v_mul_f32_e32 v79, 0x3a810204, v78
	global_store_dword v12, v79, s[40:41]
	s_branch .LBB0_339
.LBB0_342:
	s_waitcnt vmcnt(0)
	s_cmpk_gt_i32 s24, 0x3ff
	s_cbranch_scc1 .LBB0_347
	v_mbcnt_lo_u32_b32 v2, -1, 0
	v_mbcnt_hi_u32_b32 v2, -1, v2
	v_and_b32_e32 v3, 64, v2
	v_add_u32_e32 v3, 64, v3
	v_xor_b32_e32 v4, 1, v2
	v_cmp_lt_i32_e32 vcc, v4, v3
	s_ashr_i32 s25, s24, 31
	s_lshl_b64 s[0:1], s[24:25], 2
	v_cndmask_b32_e32 v4, v2, v4, vcc
	v_lshlrev_b32_e32 v6, 2, v4
	v_xor_b32_e32 v4, 2, v2
	v_cmp_lt_i32_e32 vcc, v4, v3
	s_add_u32 s10, s0, 0xcad000
	s_addc_u32 s11, s1, 0
	v_cndmask_b32_e32 v4, v2, v4, vcc
	v_lshlrev_b32_e32 v7, 2, v4
	v_xor_b32_e32 v4, 4, v2
	v_cmp_lt_i32_e32 vcc, v4, v3
	s_ashr_i32 s37, s36, 31
	s_lshl_b64 s[4:5], s[24:25], 12
	v_cndmask_b32_e32 v4, v2, v4, vcc
	v_lshlrev_b32_e32 v8, 2, v4
	v_xor_b32_e32 v4, 8, v2
	v_cmp_lt_i32_e32 vcc, v4, v3
	s_lshl_b64 s[6:7], s[24:25], 13
	v_cmp_eq_u32_e64 s[2:3], 0, v166
	v_cndmask_b32_e32 v4, v2, v4, vcc
	v_lshlrev_b32_e32 v9, 2, v4
	v_xor_b32_e32 v4, 16, v2
	v_cmp_lt_i32_e32 vcc, v4, v3
	s_lshl_b64 s[0:1], s[36:37], 2
	v_mov_b32_e32 v5, s7
	v_cndmask_b32_e32 v4, v2, v4, vcc
	v_lshlrev_b32_e32 v10, 2, v4
	v_xor_b32_e32 v4, 32, v2
	v_cmp_lt_i32_e32 vcc, v4, v3
	v_mov_b32_e32 v3, s5
	s_mov_b32 s12, 0x19201000
	v_cndmask_b32_e32 v2, v2, v4, vcc
	v_lshlrev_b32_e32 v11, 2, v2
	v_lshl_or_b32 v2, v166, 3, s4
	s_lshl_b64 s[4:5], s[36:37], 12
	v_lshl_or_b32 v4, v166, 4, s6
	s_lshl_b64 s[6:7], s[36:37], 13
	s_mov_b32 s13, 0xda24260
	v_mov_b32_e32 v12, 0
	s_mov_b32 s25, 0x42fe0000
	s_mov_b32 s33, 0x4b3fff81
	s_mov_b32 s34, 0xc0c0400
	s_mov_b32 s35, 0x4000c0c
	s_mov_b32 s37, 0x56e00000
	v_mov_b32_e32 v13, 0x4b40007f
	s_mov_b32 s38, s24
	v_lshl_add_u64 v[120:121], s[68:69], 0, v[4:5]
	v_add_co_u32_e32 v136, vcc, s12, v120
	s_nop 1
	v_addc_co_u32_e32 v137, vcc, 0, v121, vcc
	v_add_co_u32_e32 v144, vcc, 0x19200000, v120
	global_load_dwordx4 v[102:105], v[136:137], off
	global_load_dwordx4 v[106:109], v[136:137], off offset:1024
	global_load_dwordx4 v[110:113], v[136:137], off offset:2048
	s_nop 0
	global_load_dwordx4 v[116:119], v[136:137], off offset:3072
	v_addc_co_u32_e32 v145, vcc, 0, v121, vcc
	global_load_dwordx4 v[128:131], v[144:145], off
	global_load_dwordx4 v[132:135], v[144:145], off offset:1024
	global_load_dwordx4 v[168:171], v[144:145], off offset:2048
	s_nop 0
	global_load_dwordx4 v[172:175], v[144:145], off offset:3072
	s_waitcnt vmcnt(7)
	v_cvt_f32_f16_e32 v46, v102
	v_cvt_f32_f16_sdwa v14, v102 dst_sel:DWORD dst_unused:UNUSED_PAD src0_sel:WORD_1
	v_cvt_f32_f16_e32 v47, v103
	v_cvt_f32_f16_sdwa v15, v103 dst_sel:DWORD dst_unused:UNUSED_PAD src0_sel:WORD_1
	v_cvt_f32_f16_e32 v48, v104
	v_cvt_f32_f16_sdwa v16, v104 dst_sel:DWORD dst_unused:UNUSED_PAD src0_sel:WORD_1
	v_cvt_f32_f16_e32 v49, v105
	v_cvt_f32_f16_sdwa v17, v105 dst_sel:DWORD dst_unused:UNUSED_PAD src0_sel:WORD_1
	s_waitcnt vmcnt(6)
	v_cvt_f32_f16_e32 v50, v106
	v_cvt_f32_f16_sdwa v18, v106 dst_sel:DWORD dst_unused:UNUSED_PAD src0_sel:WORD_1
	v_cvt_f32_f16_e32 v51, v107
	v_cvt_f32_f16_sdwa v19, v107 dst_sel:DWORD dst_unused:UNUSED_PAD src0_sel:WORD_1
	v_cvt_f32_f16_e32 v52, v108
	v_cvt_f32_f16_sdwa v20, v108 dst_sel:DWORD dst_unused:UNUSED_PAD src0_sel:WORD_1
	v_cvt_f32_f16_e32 v53, v109
	v_cvt_f32_f16_sdwa v21, v109 dst_sel:DWORD dst_unused:UNUSED_PAD src0_sel:WORD_1
	s_waitcnt vmcnt(5)
	v_cvt_f32_f16_e32 v54, v110
	v_cvt_f32_f16_sdwa v22, v110 dst_sel:DWORD dst_unused:UNUSED_PAD src0_sel:WORD_1
	v_cvt_f32_f16_e32 v55, v111
	v_cvt_f32_f16_sdwa v23, v111 dst_sel:DWORD dst_unused:UNUSED_PAD src0_sel:WORD_1
	v_cvt_f32_f16_e32 v56, v112
	v_cvt_f32_f16_sdwa v24, v112 dst_sel:DWORD dst_unused:UNUSED_PAD src0_sel:WORD_1
	v_cvt_f32_f16_e32 v57, v113
	v_cvt_f32_f16_sdwa v25, v113 dst_sel:DWORD dst_unused:UNUSED_PAD src0_sel:WORD_1
	s_waitcnt vmcnt(4)
	v_cvt_f32_f16_e32 v58, v116
	v_cvt_f32_f16_sdwa v26, v116 dst_sel:DWORD dst_unused:UNUSED_PAD src0_sel:WORD_1
	v_cvt_f32_f16_e32 v59, v117
	v_cvt_f32_f16_sdwa v27, v117 dst_sel:DWORD dst_unused:UNUSED_PAD src0_sel:WORD_1
	v_cvt_f32_f16_e32 v60, v118
	v_cvt_f32_f16_sdwa v28, v118 dst_sel:DWORD dst_unused:UNUSED_PAD src0_sel:WORD_1
	v_cvt_f32_f16_e32 v61, v119
	v_cvt_f32_f16_sdwa v29, v119 dst_sel:DWORD dst_unused:UNUSED_PAD src0_sel:WORD_1
	s_waitcnt vmcnt(3)
	v_cvt_f32_f16_e32 v62, v128
	v_cvt_f32_f16_sdwa v30, v128 dst_sel:DWORD dst_unused:UNUSED_PAD src0_sel:WORD_1
	v_cvt_f32_f16_e32 v63, v129
	v_cvt_f32_f16_sdwa v31, v129 dst_sel:DWORD dst_unused:UNUSED_PAD src0_sel:WORD_1
	v_cvt_f32_f16_e32 v64, v130
	v_cvt_f32_f16_sdwa v32, v130 dst_sel:DWORD dst_unused:UNUSED_PAD src0_sel:WORD_1
	v_cvt_f32_f16_e32 v65, v131
	v_cvt_f32_f16_sdwa v33, v131 dst_sel:DWORD dst_unused:UNUSED_PAD src0_sel:WORD_1
	s_waitcnt vmcnt(2)
	v_cvt_f32_f16_e32 v66, v132
	v_cvt_f32_f16_sdwa v34, v132 dst_sel:DWORD dst_unused:UNUSED_PAD src0_sel:WORD_1
	v_cvt_f32_f16_e32 v67, v133
	v_cvt_f32_f16_sdwa v35, v133 dst_sel:DWORD dst_unused:UNUSED_PAD src0_sel:WORD_1
	v_cvt_f32_f16_e32 v68, v134
	v_cvt_f32_f16_sdwa v36, v134 dst_sel:DWORD dst_unused:UNUSED_PAD src0_sel:WORD_1
	v_cvt_f32_f16_e32 v69, v135
	v_cvt_f32_f16_sdwa v37, v135 dst_sel:DWORD dst_unused:UNUSED_PAD src0_sel:WORD_1
	s_waitcnt vmcnt(1)
	v_cvt_f32_f16_e32 v70, v168
	v_cvt_f32_f16_sdwa v38, v168 dst_sel:DWORD dst_unused:UNUSED_PAD src0_sel:WORD_1
	v_cvt_f32_f16_e32 v71, v169
	v_cvt_f32_f16_sdwa v39, v169 dst_sel:DWORD dst_unused:UNUSED_PAD src0_sel:WORD_1
	v_cvt_f32_f16_e32 v72, v170
	v_cvt_f32_f16_sdwa v40, v170 dst_sel:DWORD dst_unused:UNUSED_PAD src0_sel:WORD_1
	v_cvt_f32_f16_e32 v73, v171
	v_cvt_f32_f16_sdwa v41, v171 dst_sel:DWORD dst_unused:UNUSED_PAD src0_sel:WORD_1
	s_waitcnt vmcnt(0)
	v_cvt_f32_f16_e32 v74, v172
	v_cvt_f32_f16_sdwa v42, v172 dst_sel:DWORD dst_unused:UNUSED_PAD src0_sel:WORD_1
	v_cvt_f32_f16_e32 v75, v173
	v_cvt_f32_f16_sdwa v43, v173 dst_sel:DWORD dst_unused:UNUSED_PAD src0_sel:WORD_1
	v_cvt_f32_f16_e32 v76, v174
	v_cvt_f32_f16_sdwa v44, v174 dst_sel:DWORD dst_unused:UNUSED_PAD src0_sel:WORD_1
	v_cvt_f32_f16_e32 v77, v175
	v_cvt_f32_f16_sdwa v45, v175 dst_sel:DWORD dst_unused:UNUSED_PAD src0_sel:WORD_1
	s_branch .Lrp_q2_go

.Lrp_q2_go:
	v_lshl_add_u64 v[120:121], v[4:5], 0, s[6:7]
	v_lshl_add_u64 v[120:121], s[68:69], 0, v[120:121]
	v_add_co_u32_e32 v136, vcc, s12, v120
	s_nop 1
	v_addc_co_u32_e32 v137, vcc, 0, v121, vcc
	v_add_co_u32_e32 v144, vcc, 0x19200000, v120
	global_load_dwordx4 v[102:105], v[136:137], off
	global_load_dwordx4 v[106:109], v[136:137], off offset:1024
	global_load_dwordx4 v[110:113], v[136:137], off offset:2048
	s_nop 0
	global_load_dwordx4 v[116:119], v[136:137], off offset:3072
	v_addc_co_u32_e32 v145, vcc, 0, v121, vcc
	global_load_dwordx4 v[128:131], v[144:145], off
	global_load_dwordx4 v[132:135], v[144:145], off offset:1024
	global_load_dwordx4 v[168:171], v[144:145], off offset:2048
	s_nop 0
	global_load_dwordx4 v[172:175], v[144:145], off offset:3072
	v_add_f32_e32 v78, v62, v30
	v_sub_f32_e32 v30, v62, v30
	v_add_f32_e32 v62, v63, v31
	v_sub_f32_e32 v31, v63, v31
	v_add_f32_e32 v63, v64, v32
	v_sub_f32_e32 v32, v64, v32
	v_add_f32_e32 v64, v65, v33
	v_sub_f32_e32 v33, v65, v33
	v_add_f32_e32 v65, v66, v34
	v_sub_f32_e32 v34, v66, v34
	v_add_f32_e32 v66, v67, v35
	v_sub_f32_e32 v35, v67, v35
	v_add_f32_e32 v67, v68, v36
	v_sub_f32_e32 v36, v68, v36
	v_add_f32_e32 v68, v69, v37
	v_sub_f32_e32 v37, v69, v37
	v_add_f32_e32 v69, v70, v38
	v_sub_f32_e32 v38, v70, v38
	v_add_f32_e32 v70, v71, v39
	v_sub_f32_e32 v39, v71, v39
	v_add_f32_e32 v71, v72, v40
	v_sub_f32_e32 v40, v72, v40
	v_add_f32_e32 v72, v73, v41
	v_sub_f32_e32 v41, v73, v41
	v_add_f32_e32 v73, v74, v42
	v_sub_f32_e32 v42, v74, v42
	v_add_f32_e32 v74, v75, v43
	v_sub_f32_e32 v43, v75, v43
	v_add_f32_e32 v75, v76, v44
	v_sub_f32_e32 v44, v76, v44
	v_add_f32_e32 v76, v77, v45
	v_sub_f32_e32 v45, v77, v45
	v_add_f32_e32 v77, v46, v14
	v_sub_f32_e32 v14, v46, v14
	v_add_f32_e32 v46, v47, v15
	v_sub_f32_e32 v15, v47, v15
	v_add_f32_e32 v47, v48, v16
	v_sub_f32_e32 v16, v48, v16
	v_add_f32_e32 v48, v49, v17
	v_sub_f32_e32 v17, v49, v17
	v_add_f32_e32 v49, v50, v18
	v_sub_f32_e32 v18, v50, v18
	v_add_f32_e32 v50, v51, v19
	v_sub_f32_e32 v19, v51, v19
	v_add_f32_e32 v51, v52, v20
	v_sub_f32_e32 v20, v52, v20
	v_add_f32_e32 v52, v53, v21
	v_sub_f32_e32 v21, v53, v21
	v_add_f32_e32 v53, v54, v22
	v_sub_f32_e32 v22, v54, v22
	v_add_f32_e32 v54, v55, v23
	v_sub_f32_e32 v23, v55, v23
	v_add_f32_e32 v55, v56, v24
	v_sub_f32_e32 v24, v56, v24
	v_add_f32_e32 v56, v57, v25
	v_sub_f32_e32 v25, v57, v25
	v_add_f32_e32 v57, v58, v26
	v_sub_f32_e32 v26, v58, v26
	v_add_f32_e32 v58, v59, v27
	v_sub_f32_e32 v27, v59, v27
	v_add_f32_e32 v59, v60, v28
	v_sub_f32_e32 v28, v60, v28
	v_add_f32_e32 v60, v61, v29
	v_sub_f32_e32 v29, v61, v29
	v_add_f32_e32 v61, v78, v62
	v_sub_f32_e32 v62, v78, v62
	v_add_f32_e32 v78, v30, v31
	v_sub_f32_e32 v30, v30, v31
	v_add_f32_e32 v31, v63, v64
	v_sub_f32_e32 v63, v63, v64
	v_add_f32_e32 v64, v32, v33
	v_sub_f32_e32 v32, v32, v33
	v_add_f32_e32 v33, v65, v66
	v_sub_f32_e32 v65, v65, v66
	v_add_f32_e32 v66, v34, v35
	v_sub_f32_e32 v34, v34, v35
	v_add_f32_e32 v35, v67, v68
	v_sub_f32_e32 v67, v67, v68
	v_add_f32_e32 v68, v36, v37
	v_sub_f32_e32 v36, v36, v37
	v_add_f32_e32 v37, v69, v70
	v_sub_f32_e32 v69, v69, v70
	v_add_f32_e32 v70, v38, v39
	v_sub_f32_e32 v38, v38, v39
	v_add_f32_e32 v39, v71, v72
	v_sub_f32_e32 v71, v71, v72
	v_add_f32_e32 v72, v40, v41
	v_sub_f32_e32 v40, v40, v41
	v_add_f32_e32 v41, v73, v74
	v_sub_f32_e32 v73, v73, v74
	v_add_f32_e32 v74, v42, v43
	v_sub_f32_e32 v42, v42, v43
	v_add_f32_e32 v43, v75, v76
	v_sub_f32_e32 v75, v75, v76
	v_add_f32_e32 v76, v44, v45
	v_sub_f32_e32 v44, v44, v45
	v_add_f32_e32 v45, v77, v46
	v_sub_f32_e32 v46, v77, v46
	v_add_f32_e32 v77, v14, v15
	v_sub_f32_e32 v14, v14, v15
	v_add_f32_e32 v15, v47, v48
	v_sub_f32_e32 v47, v47, v48
	v_add_f32_e32 v48, v16, v17
	v_sub_f32_e32 v16, v16, v17
	v_add_f32_e32 v17, v49, v50
	v_sub_f32_e32 v49, v49, v50
	v_add_f32_e32 v50, v18, v19
	v_sub_f32_e32 v18, v18, v19
	v_add_f32_e32 v19, v51, v52
	v_sub_f32_e32 v51, v51, v52
	v_add_f32_e32 v52, v20, v21
	v_sub_f32_e32 v20, v20, v21
	v_add_f32_e32 v21, v53, v54
	v_sub_f32_e32 v53, v53, v54
	v_add_f32_e32 v54, v22, v23
	v_sub_f32_e32 v22, v22, v23
	v_add_f32_e32 v23, v55, v56
	v_sub_f32_e32 v55, v55, v56
	v_add_f32_e32 v56, v24, v25
	v_sub_f32_e32 v24, v24, v25
	v_add_f32_e32 v25, v57, v58
	v_sub_f32_e32 v57, v57, v58
	v_add_f32_e32 v58, v26, v27
	v_sub_f32_e32 v26, v26, v27
	v_add_f32_e32 v27, v59, v60
	v_sub_f32_e32 v59, v59, v60
	v_add_f32_e32 v60, v28, v29
	v_sub_f32_e32 v28, v28, v29
	v_add_f32_e32 v29, v61, v31
	v_sub_f32_e32 v31, v61, v31
	v_add_f32_e32 v61, v78, v64
	v_sub_f32_e32 v64, v78, v64
	v_add_f32_e32 v78, v62, v63
	v_sub_f32_e32 v62, v62, v63
	v_add_f32_e32 v63, v30, v32
	v_sub_f32_e32 v30, v30, v32
	v_add_f32_e32 v32, v33, v35
	v_sub_f32_e32 v33, v33, v35
	v_add_f32_e32 v35, v66, v68
	v_sub_f32_e32 v66, v66, v68
	v_add_f32_e32 v68, v65, v67
	v_sub_f32_e32 v65, v65, v67
	v_add_f32_e32 v67, v34, v36
	v_sub_f32_e32 v34, v34, v36
	v_add_f32_e32 v36, v37, v39
	v_sub_f32_e32 v37, v37, v39
	v_add_f32_e32 v39, v70, v72
	v_sub_f32_e32 v70, v70, v72
	v_add_f32_e32 v72, v69, v71
	v_sub_f32_e32 v69, v69, v71
	v_add_f32_e32 v71, v38, v40
	v_sub_f32_e32 v38, v38, v40
	v_add_f32_e32 v40, v41, v43
	v_sub_f32_e32 v41, v41, v43
	v_add_f32_e32 v43, v74, v76
	v_sub_f32_e32 v74, v74, v76
	v_add_f32_e32 v76, v73, v75
	v_sub_f32_e32 v73, v73, v75
	v_add_f32_e32 v75, v42, v44
	v_sub_f32_e32 v42, v42, v44
	v_add_f32_e32 v44, v45, v15
	v_sub_f32_e32 v15, v45, v15
	v_add_f32_e32 v45, v77, v48
	v_sub_f32_e32 v48, v77, v48
	v_add_f32_e32 v77, v46, v47
	v_sub_f32_e32 v46, v46, v47
	v_add_f32_e32 v47, v14, v16
	v_sub_f32_e32 v14, v14, v16
	v_add_f32_e32 v16, v17, v19
	v_sub_f32_e32 v17, v17, v19
	v_add_f32_e32 v19, v50, v52
	v_sub_f32_e32 v50, v50, v52
	v_add_f32_e32 v52, v49, v51
	v_sub_f32_e32 v49, v49, v51
	v_add_f32_e32 v51, v18, v20
	v_sub_f32_e32 v18, v18, v20
	v_add_f32_e32 v20, v21, v23
	v_sub_f32_e32 v21, v21, v23
	v_add_f32_e32 v23, v54, v56
	v_sub_f32_e32 v54, v54, v56
	v_add_f32_e32 v56, v53, v55
	v_sub_f32_e32 v53, v53, v55
	v_add_f32_e32 v55, v22, v24
	v_sub_f32_e32 v22, v22, v24
	v_add_f32_e32 v24, v25, v27
	v_sub_f32_e32 v25, v25, v27
	v_add_f32_e32 v27, v58, v60
	v_sub_f32_e32 v58, v58, v60
	v_add_f32_e32 v60, v57, v59
	v_sub_f32_e32 v57, v57, v59
	v_add_f32_e32 v59, v26, v28
	v_sub_f32_e32 v26, v26, v28
	v_add_f32_e32 v28, v29, v32
	v_sub_f32_e32 v29, v29, v32
	v_add_f32_e32 v32, v61, v35
	v_sub_f32_e32 v35, v61, v35
	v_add_f32_e32 v61, v78, v68
	v_sub_f32_e32 v68, v78, v68
	v_add_f32_e32 v78, v63, v67
	v_sub_f32_e32 v63, v63, v67
	v_add_f32_e32 v67, v31, v33
	v_sub_f32_e32 v31, v31, v33
	v_add_f32_e32 v33, v64, v66
	v_sub_f32_e32 v64, v64, v66
	v_add_f32_e32 v66, v62, v65
	v_sub_f32_e32 v62, v62, v65
	v_add_f32_e32 v65, v30, v34
	v_sub_f32_e32 v30, v30, v34
	v_add_f32_e32 v34, v36, v40
	v_sub_f32_e32 v36, v36, v40
	v_add_f32_e32 v40, v39, v43
	v_sub_f32_e32 v39, v39, v43
	v_add_f32_e32 v43, v72, v76
	v_sub_f32_e32 v72, v72, v76
	v_add_f32_e32 v76, v71, v75
	v_sub_f32_e32 v71, v71, v75
	v_add_f32_e32 v75, v37, v41
	v_sub_f32_e32 v37, v37, v41
	v_add_f32_e32 v41, v70, v74
	v_sub_f32_e32 v70, v70, v74
	v_add_f32_e32 v74, v69, v73
	v_sub_f32_e32 v69, v69, v73
	v_add_f32_e32 v73, v38, v42
	v_sub_f32_e32 v38, v38, v42
	v_add_f32_e32 v42, v44, v16
	v_sub_f32_e32 v16, v44, v16
	v_add_f32_e32 v44, v45, v19
	v_sub_f32_e32 v19, v45, v19
	v_add_f32_e32 v45, v77, v52
	v_sub_f32_e32 v52, v77, v52
	v_add_f32_e32 v77, v47, v51
	v_sub_f32_e32 v47, v47, v51
	v_add_f32_e32 v51, v15, v17
	v_sub_f32_e32 v15, v15, v17
	v_add_f32_e32 v17, v48, v50
	v_sub_f32_e32 v48, v48, v50
	v_add_f32_e32 v50, v46, v49
	v_sub_f32_e32 v46, v46, v49
	v_add_f32_e32 v49, v14, v18
	v_sub_f32_e32 v14, v14, v18
	v_add_f32_e32 v18, v20, v24
	v_sub_f32_e32 v20, v20, v24
	v_add_f32_e32 v24, v23, v27
	v_sub_f32_e32 v23, v23, v27
	v_add_f32_e32 v27, v56, v60
	v_sub_f32_e32 v56, v56, v60
	v_add_f32_e32 v60, v55, v59
	v_sub_f32_e32 v55, v55, v59
	v_add_f32_e32 v59, v21, v25
	v_sub_f32_e32 v21, v21, v25
	v_add_f32_e32 v25, v54, v58
	v_sub_f32_e32 v54, v54, v58
	v_add_f32_e32 v58, v53, v57
	v_sub_f32_e32 v53, v53, v57
	v_add_f32_e32 v57, v22, v26
	v_sub_f32_e32 v22, v22, v26
	v_add_f32_e32 v26, v28, v34
	v_sub_f32_e32 v28, v28, v34
	v_add_f32_e32 v34, v32, v40
	v_add_f32_e32 v80, v67, v75
	v_sub_f32_e32 v81, v67, v75
	v_add_f32_e32 v67, v33, v41
	v_sub_f32_e32 v82, v33, v41
	v_add_f32_e32 v41, v65, v73
	v_sub_f32_e32 v84, v65, v73
	v_add_f32_e32 v65, v29, v36
	v_sub_f32_e32 v85, v29, v36
	v_add_f32_e32 v29, v35, v39
	v_sub_f32_e32 v86, v35, v39
	v_add_f32_e32 v94, v30, v38
	v_sub_f32_e32 v95, v30, v38
	v_add_f32_e32 v30, v42, v18
	v_add_f32_e32 v35, v44, v24
	v_sub_f32_e32 v79, v32, v40
	v_add_f32_e32 v32, v61, v43
	v_sub_f32_e32 v61, v61, v43
	v_add_f32_e32 v40, v78, v76
	v_sub_f32_e32 v78, v78, v76
	v_add_f32_e32 v33, v66, v74
	v_sub_f32_e32 v83, v66, v74
	v_add_f32_e32 v88, v63, v71
	v_sub_f32_e32 v89, v63, v71
	v_add_f32_e32 v63, v31, v37
	v_sub_f32_e32 v90, v31, v37
	v_sub_f32_e32 v18, v42, v18
	v_add_f32_e32 v37, v45, v27
	v_sub_f32_e32 v96, v45, v27
	v_add_f32_e32 v27, v77, v60
	v_sub_f32_e32 v97, v77, v60
	v_add_f32_e32 v39, v17, v25
	v_sub_f32_e32 v17, v17, v25
	v_add_f32_e32 v25, v50, v58
	v_sub_f32_e32 v50, v50, v58
	v_add_f32_e32 v58, v49, v57
	v_sub_f32_e32 v49, v49, v57
	v_add_f32_e32 v57, v16, v20
	v_sub_f32_e32 v16, v16, v20
	v_add_f32_e32 v20, v19, v23
	v_add_f32_e32 v74, v26, v30
	v_add_f32_e32 v75, v34, v35
	v_add_f32_e32 v38, v51, v59
	v_sub_f32_e32 v42, v26, v30
	v_sub_f32_e32 v43, v34, v35
	v_add_f32_e32 v76, v32, v37
	v_add_f32_e32 v77, v40, v27
	v_add_f32_e32 v71, v67, v39
	v_sub_f32_e32 v39, v67, v39
	v_add_f32_e32 v73, v41, v58
	v_sub_f32_e32 v41, v41, v58
	v_add_f32_e32 v67, v29, v20
	v_sub_f32_e32 v35, v29, v20
	v_add_f32_e32 v58, v28, v18
	v_sub_f32_e32 v26, v28, v18
	v_add_f32_e32 v60, v61, v96
	v_sub_f32_e32 v28, v61, v96
	v_add_f32_e32 v61, v78, v97
	v_sub_f32_e32 v29, v78, v97
	v_max3_f32 v78, |v74|, 0, |v75|
	v_add_f32_e32 v31, v64, v70
	v_sub_f32_e32 v91, v64, v70
	v_add_f32_e32 v70, v80, v38
	v_max3_f32 v78, v78, |v76|, |v77|
	v_add_f32_e32 v36, v68, v72
	v_sub_f32_e32 v87, v68, v72
	v_add_f32_e32 v72, v33, v25
	v_max3_f32 v78, v78, |v70|, |v71|
	v_sub_f32_e32 v19, v19, v23
	v_add_f32_e32 v23, v52, v56
	v_sub_f32_e32 v98, v52, v56
	v_add_f32_e32 v52, v47, v55
	v_add_f32_e32 v66, v65, v57
	v_max3_f32 v78, v78, |v72|, |v73|
	v_add_f32_e32 v92, v62, v69
	v_sub_f32_e32 v93, v62, v69
	v_sub_f32_e32 v47, v47, v55
	v_add_f32_e32 v55, v15, v21
	v_sub_f32_e32 v15, v15, v21
	v_add_f32_e32 v21, v48, v54
	v_add_f32_e32 v68, v36, v23
	v_add_f32_e32 v69, v88, v52
	v_max3_f32 v78, v78, |v66|, |v67|
	v_sub_f32_e32 v48, v48, v54
	v_add_f32_e32 v54, v46, v53
	v_sub_f32_e32 v99, v46, v53
	v_add_f32_e32 v46, v14, v22
	v_add_f32_e32 v62, v63, v55
	v_sub_f32_e32 v30, v63, v55
	v_add_f32_e32 v63, v31, v21
	v_max3_f32 v78, v78, |v68|, |v69|
	v_sub_f32_e32 v24, v44, v24
	v_sub_f32_e32 v34, v65, v57
	v_add_f32_e32 v64, v92, v54
	v_add_f32_e32 v65, v94, v46
	v_max3_f32 v78, v78, |v62|, |v63|
	v_sub_f32_e32 v51, v51, v59
	v_add_f32_e32 v59, v79, v24
	v_max3_f32 v78, v78, |v64|, |v65|
	v_max3_f32 v78, v78, |v58|, |v59|
	v_sub_f32_e32 v44, v32, v37
	v_sub_f32_e32 v32, v92, v54
	v_add_f32_e32 v54, v81, v51
	v_add_f32_e32 v55, v82, v17
	v_max3_f32 v78, v78, |v60|, |v61|
	v_add_f32_e32 v56, v83, v50
	v_add_f32_e32 v57, v84, v49
	v_max3_f32 v78, v78, |v54|, |v55|
	v_sub_f32_e32 v100, v14, v22
	v_sub_f32_e32 v45, v40, v27
	v_sub_f32_e32 v27, v79, v24
	v_sub_f32_e32 v22, v81, v51
	v_sub_f32_e32 v24, v83, v50
	v_add_f32_e32 v50, v85, v16
	v_add_f32_e32 v51, v86, v19
	v_max3_f32 v78, v78, |v56|, |v57|
	v_sub_f32_e32 v37, v88, v52
	v_add_f32_e32 v52, v87, v98
	v_add_f32_e32 v53, v89, v47
	v_max3_f32 v78, v78, |v50|, |v51|
	v_sub_f32_e32 v40, v33, v25
	v_sub_f32_e32 v31, v31, v21
	v_sub_f32_e32 v33, v94, v46
	v_sub_f32_e32 v21, v89, v47
	v_add_f32_e32 v46, v90, v15
	v_add_f32_e32 v47, v91, v48
	v_max3_f32 v78, v78, |v52|, |v53|
	v_sub_f32_e32 v25, v84, v49
	v_sub_f32_e32 v14, v90, v15
	v_sub_f32_e32 v15, v91, v48
	v_add_f32_e32 v48, v93, v99
	v_add_f32_e32 v49, v95, v100
	v_max3_f32 v78, v78, |v46|, |v47|
	v_max3_f32 v78, v78, |v48|, |v49|
	v_max3_f32 v78, v78, |v42|, |v43|
	v_sub_f32_e32 v38, v80, v38
	v_max3_f32 v78, v78, |v44|, |v45|
	v_max3_f32 v78, v78, |v38|, |v39|
	v_max3_f32 v78, v78, |v40|, |v41|
	v_sub_f32_e32 v36, v36, v23
	v_max3_f32 v78, v78, |v34|, |v35|
	v_max3_f32 v78, v78, |v36|, |v37|
	v_max3_f32 v78, v78, |v30|, |v31|
	v_max3_f32 v78, v78, |v32|, |v33|
	v_max3_f32 v78, v78, |v26|, |v27|
	v_sub_f32_e32 v23, v82, v17
	v_max3_f32 v78, v78, |v28|, |v29|
	v_max3_f32 v78, v78, |v22|, |v23|
	v_sub_f32_e32 v18, v85, v16
	v_sub_f32_e32 v19, v86, v19
	v_max3_f32 v78, v78, |v24|, |v25|
	v_sub_f32_e32 v20, v87, v98
	v_max3_f32 v78, v78, |v18|, |v19|
	v_max3_f32 v78, v78, |v20|, |v21|
	v_sub_f32_e32 v16, v93, v99
	v_sub_f32_e32 v17, v95, v100
	v_max3_f32 v78, v78, |v14|, |v15|
	v_max3_f32 v78, v78, |v16|, |v17|
	ds_bpermute_b32 v79, v6, v78
	s_waitcnt lgkmcnt(0)
	v_max_f32_e32 v79, v79, v79
	v_max_f32_e32 v78, v78, v79
	ds_bpermute_b32 v79, v7, v78
	s_waitcnt lgkmcnt(0)
	v_max_f32_e32 v79, v79, v79
	v_max_f32_e32 v78, v78, v79
	ds_bpermute_b32 v79, v8, v78
	s_waitcnt lgkmcnt(0)
	v_max_f32_e32 v79, v79, v79
	v_max_f32_e32 v78, v78, v79
	ds_bpermute_b32 v79, v9, v78
	s_waitcnt lgkmcnt(0)
	v_max_f32_e32 v79, v79, v79
	v_max_f32_e32 v78, v78, v79
	ds_bpermute_b32 v79, v10, v78
	s_waitcnt lgkmcnt(0)
	v_max_f32_e32 v79, v79, v79
	v_max_f32_e32 v78, v78, v79
	ds_bpermute_b32 v79, v11, v78
	s_waitcnt lgkmcnt(0)
	v_max3_f32 v78, v78, v79, s13
	s_and_saveexec_b64 s[8:9], s[2:3]
	s_cbranch_execz .LBB0_344
	s_add_u32 s40, s68, s10
	s_addc_u32 s41, s69, s11
	v_mul_f32_e32 v79, 0x3a810204, v78
	global_store_dword v12, v79, s[40:41]
	s_branch .LBB0_344
.LBB0_347:
	s_waitcnt vmcnt(0)
	s_cmpk_gt_i32 s24, 0x55ff
	s_cbranch_scc1 .LBB0_352
	v_mbcnt_lo_u32_b32 v2, -1, 0
	v_mbcnt_hi_u32_b32 v2, -1, v2
	v_and_b32_e32 v3, 64, v2
	v_add_u32_e32 v3, 64, v3
	v_xor_b32_e32 v4, 1, v2
	v_cmp_lt_i32_e32 vcc, v4, v3
	s_ashr_i32 s25, s24, 31
	s_lshl_b64 s[0:1], s[24:25], 2
	v_cndmask_b32_e32 v4, v2, v4, vcc
	v_lshlrev_b32_e32 v6, 2, v4
	v_xor_b32_e32 v4, 2, v2
	v_cmp_lt_i32_e32 vcc, v4, v3
	s_add_u32 s10, s0, 0xc40000
	s_addc_u32 s11, s1, 0
	v_cndmask_b32_e32 v4, v2, v4, vcc
	v_lshlrev_b32_e32 v7, 2, v4
	v_xor_b32_e32 v4, 4, v2
	v_cmp_lt_i32_e32 vcc, v4, v3
	s_ashr_i32 s37, s36, 31
	s_lshl_b64 s[4:5], s[24:25], 12
	v_cndmask_b32_e32 v4, v2, v4, vcc
	v_lshlrev_b32_e32 v8, 2, v4
	v_xor_b32_e32 v4, 8, v2
	v_cmp_lt_i32_e32 vcc, v4, v3
	s_lshl_b64 s[6:7], s[24:25], 13
	v_cmp_eq_u32_e64 s[2:3], 0, v166
	v_cndmask_b32_e32 v4, v2, v4, vcc
	v_lshlrev_b32_e32 v9, 2, v4
	v_xor_b32_e32 v4, 16, v2
	v_cmp_lt_i32_e32 vcc, v4, v3
	s_lshl_b64 s[0:1], s[36:37], 2
	v_mov_b32_e32 v5, s7
	v_cndmask_b32_e32 v4, v2, v4, vcc
	v_lshlrev_b32_e32 v10, 2, v4
	v_xor_b32_e32 v4, 32, v2
	v_cmp_lt_i32_e32 vcc, v4, v3
	v_mov_b32_e32 v3, s5
	s_mov_b32 s12, 0x1001000
	v_cndmask_b32_e32 v2, v2, v4, vcc
	v_lshlrev_b32_e32 v11, 2, v2
	v_lshl_or_b32 v2, v166, 3, s4
	s_lshl_b64 s[4:5], s[36:37], 12
	v_lshl_or_b32 v4, v166, 4, s6
	s_lshl_b64 s[6:7], s[36:37], 13
	s_mov_b32 s13, 0xda24260
	v_mov_b32_e32 v12, 0
	s_mov_b32 s25, 0x42fe0000
	s_mov_b32 s33, 0x4b3fff81
	s_mov_b32 s34, 0xc0c0400
	s_mov_b32 s35, 0x4000c0c
	s_mov_b32 s37, 0x59a00000
	v_mov_b32_e32 v13, 0x4b40007f
	v_lshl_add_u64 v[120:121], s[68:69], 0, v[4:5]
	v_add_co_u32_e32 v136, vcc, s12, v120
	s_nop 1
	v_addc_co_u32_e32 v137, vcc, 0, v121, vcc
	v_add_co_u32_e32 v144, vcc, 0x1000000, v120
	global_load_dwordx4 v[102:105], v[136:137], off
	global_load_dwordx4 v[106:109], v[136:137], off offset:1024
	global_load_dwordx4 v[110:113], v[136:137], off offset:2048
	s_nop 0
	global_load_dwordx4 v[116:119], v[136:137], off offset:3072
	v_addc_co_u32_e32 v145, vcc, 0, v121, vcc
	global_load_dwordx4 v[128:131], v[144:145], off
	global_load_dwordx4 v[132:135], v[144:145], off offset:1024
	global_load_dwordx4 v[168:171], v[144:145], off offset:2048
	s_nop 0
	global_load_dwordx4 v[172:175], v[144:145], off offset:3072
	s_waitcnt vmcnt(7)
	v_lshlrev_b32_e32 v46, 16, v102
	v_and_b32_e32 v14, 0xffff0000, v102
	v_lshlrev_b32_e32 v47, 16, v103
	v_and_b32_e32 v15, 0xffff0000, v103
	v_lshlrev_b32_e32 v48, 16, v104
	v_and_b32_e32 v16, 0xffff0000, v104
	v_lshlrev_b32_e32 v49, 16, v105
	v_and_b32_e32 v17, 0xffff0000, v105
	s_waitcnt vmcnt(6)
	v_lshlrev_b32_e32 v50, 16, v106
	v_and_b32_e32 v18, 0xffff0000, v106
	v_lshlrev_b32_e32 v51, 16, v107
	v_and_b32_e32 v19, 0xffff0000, v107
	v_lshlrev_b32_e32 v52, 16, v108
	v_and_b32_e32 v20, 0xffff0000, v108
	v_lshlrev_b32_e32 v53, 16, v109
	v_and_b32_e32 v21, 0xffff0000, v109
	s_waitcnt vmcnt(5)
	v_lshlrev_b32_e32 v54, 16, v110
	v_and_b32_e32 v22, 0xffff0000, v110
	v_lshlrev_b32_e32 v55, 16, v111
	v_and_b32_e32 v23, 0xffff0000, v111
	v_lshlrev_b32_e32 v56, 16, v112
	v_and_b32_e32 v24, 0xffff0000, v112
	v_lshlrev_b32_e32 v57, 16, v113
	v_and_b32_e32 v25, 0xffff0000, v113
	s_waitcnt vmcnt(4)
	v_lshlrev_b32_e32 v58, 16, v116
	v_and_b32_e32 v26, 0xffff0000, v116
	v_lshlrev_b32_e32 v59, 16, v117
	v_and_b32_e32 v27, 0xffff0000, v117
	v_lshlrev_b32_e32 v60, 16, v118
	v_and_b32_e32 v28, 0xffff0000, v118
	v_lshlrev_b32_e32 v61, 16, v119
	v_and_b32_e32 v29, 0xffff0000, v119
	s_waitcnt vmcnt(3)
	v_lshlrev_b32_e32 v62, 16, v128
	v_and_b32_e32 v30, 0xffff0000, v128
	v_lshlrev_b32_e32 v63, 16, v129
	v_and_b32_e32 v31, 0xffff0000, v129
	v_lshlrev_b32_e32 v64, 16, v130
	v_and_b32_e32 v32, 0xffff0000, v130
	v_lshlrev_b32_e32 v65, 16, v131
	v_and_b32_e32 v33, 0xffff0000, v131
	s_waitcnt vmcnt(2)
	v_lshlrev_b32_e32 v66, 16, v132
	v_and_b32_e32 v34, 0xffff0000, v132
	v_lshlrev_b32_e32 v67, 16, v133
	v_and_b32_e32 v35, 0xffff0000, v133
	v_lshlrev_b32_e32 v68, 16, v134
	v_and_b32_e32 v36, 0xffff0000, v134
	v_lshlrev_b32_e32 v69, 16, v135
	v_and_b32_e32 v37, 0xffff0000, v135
	s_waitcnt vmcnt(1)
	v_lshlrev_b32_e32 v70, 16, v168
	v_and_b32_e32 v38, 0xffff0000, v168
	v_lshlrev_b32_e32 v71, 16, v169
	v_and_b32_e32 v39, 0xffff0000, v169
	v_lshlrev_b32_e32 v72, 16, v170
	v_and_b32_e32 v40, 0xffff0000, v170
	v_lshlrev_b32_e32 v73, 16, v171
	v_and_b32_e32 v41, 0xffff0000, v171
	s_waitcnt vmcnt(0)
	v_lshlrev_b32_e32 v74, 16, v172
	v_and_b32_e32 v42, 0xffff0000, v172
	v_lshlrev_b32_e32 v75, 16, v173
	v_and_b32_e32 v43, 0xffff0000, v173
	v_lshlrev_b32_e32 v76, 16, v174
	v_and_b32_e32 v44, 0xffff0000, v174
	v_lshlrev_b32_e32 v77, 16, v175
	v_and_b32_e32 v45, 0xffff0000, v175
	s_branch .Lrp_q3_go

.LBB0_350:
	s_waitcnt vmcnt(16)
	v_lshlrev_b32_e32 v46, 16, v102
	v_and_b32_e32 v14, 0xffff0000, v102
	v_lshlrev_b32_e32 v47, 16, v103
	v_and_b32_e32 v15, 0xffff0000, v103
	v_lshlrev_b32_e32 v48, 16, v104
	v_and_b32_e32 v16, 0xffff0000, v104
	v_lshlrev_b32_e32 v49, 16, v105
	v_and_b32_e32 v17, 0xffff0000, v105
	s_waitcnt vmcnt(15)
	v_lshlrev_b32_e32 v50, 16, v106
	v_and_b32_e32 v18, 0xffff0000, v106
	v_lshlrev_b32_e32 v51, 16, v107
	v_and_b32_e32 v19, 0xffff0000, v107
	v_lshlrev_b32_e32 v52, 16, v108
	v_and_b32_e32 v20, 0xffff0000, v108
	v_lshlrev_b32_e32 v53, 16, v109
	v_and_b32_e32 v21, 0xffff0000, v109
	s_waitcnt vmcnt(14)
	v_lshlrev_b32_e32 v54, 16, v110
	v_and_b32_e32 v22, 0xffff0000, v110
	v_lshlrev_b32_e32 v55, 16, v111
	v_and_b32_e32 v23, 0xffff0000, v111
	v_lshlrev_b32_e32 v56, 16, v112
	v_and_b32_e32 v24, 0xffff0000, v112
	v_lshlrev_b32_e32 v57, 16, v113
	v_and_b32_e32 v25, 0xffff0000, v113
	s_waitcnt vmcnt(13)
	v_lshlrev_b32_e32 v58, 16, v116
	v_and_b32_e32 v26, 0xffff0000, v116
	v_lshlrev_b32_e32 v59, 16, v117
	v_and_b32_e32 v27, 0xffff0000, v117
	v_lshlrev_b32_e32 v60, 16, v118
	v_and_b32_e32 v28, 0xffff0000, v118
	v_lshlrev_b32_e32 v61, 16, v119
	v_and_b32_e32 v29, 0xffff0000, v119
	s_waitcnt vmcnt(12)
	v_lshlrev_b32_e32 v62, 16, v128
	v_and_b32_e32 v30, 0xffff0000, v128
	v_lshlrev_b32_e32 v63, 16, v129
	v_and_b32_e32 v31, 0xffff0000, v129
	v_lshlrev_b32_e32 v64, 16, v130
	v_and_b32_e32 v32, 0xffff0000, v130
	v_lshlrev_b32_e32 v65, 16, v131
	v_and_b32_e32 v33, 0xffff0000, v131
	s_waitcnt vmcnt(11)
	v_lshlrev_b32_e32 v66, 16, v132
	v_and_b32_e32 v34, 0xffff0000, v132
	v_lshlrev_b32_e32 v67, 16, v133
	v_and_b32_e32 v35, 0xffff0000, v133
	v_lshlrev_b32_e32 v68, 16, v134
	v_and_b32_e32 v36, 0xffff0000, v134
	v_lshlrev_b32_e32 v69, 16, v135
	v_and_b32_e32 v37, 0xffff0000, v135
	s_waitcnt vmcnt(10)
	v_lshlrev_b32_e32 v70, 16, v168
	v_and_b32_e32 v38, 0xffff0000, v168
	v_lshlrev_b32_e32 v71, 16, v169
	v_and_b32_e32 v39, 0xffff0000, v169
	v_lshlrev_b32_e32 v72, 16, v170
	v_and_b32_e32 v40, 0xffff0000, v170
	v_lshlrev_b32_e32 v73, 16, v171
	v_and_b32_e32 v41, 0xffff0000, v171
	s_waitcnt vmcnt(9)
	v_lshlrev_b32_e32 v74, 16, v172
	v_and_b32_e32 v42, 0xffff0000, v172
	v_lshlrev_b32_e32 v75, 16, v173
	v_and_b32_e32 v43, 0xffff0000, v173
	v_lshlrev_b32_e32 v76, 16, v174
	v_and_b32_e32 v44, 0xffff0000, v174
	v_lshlrev_b32_e32 v77, 16, v175
	v_and_b32_e32 v45, 0xffff0000, v175
.Lrp_q3_go:
	v_lshl_add_u64 v[120:121], v[4:5], 0, s[6:7]
	v_lshl_add_u64 v[120:121], s[68:69], 0, v[120:121]
	v_add_co_u32_e32 v136, vcc, s12, v120
	s_nop 1
	v_addc_co_u32_e32 v137, vcc, 0, v121, vcc
	v_add_co_u32_e32 v144, vcc, 0x1000000, v120
	global_load_dwordx4 v[102:105], v[136:137], off
	global_load_dwordx4 v[106:109], v[136:137], off offset:1024
	global_load_dwordx4 v[110:113], v[136:137], off offset:2048
	s_nop 0
	global_load_dwordx4 v[116:119], v[136:137], off offset:3072
	v_addc_co_u32_e32 v145, vcc, 0, v121, vcc
	global_load_dwordx4 v[128:131], v[144:145], off
	global_load_dwordx4 v[132:135], v[144:145], off offset:1024
	global_load_dwordx4 v[168:171], v[144:145], off offset:2048
	s_nop 0
	global_load_dwordx4 v[172:175], v[144:145], off offset:3072
	v_add_f32_e32 v78, v62, v30
	v_sub_f32_e32 v30, v62, v30
	v_add_f32_e32 v62, v63, v31
	v_sub_f32_e32 v31, v63, v31
	v_add_f32_e32 v63, v64, v32
	v_sub_f32_e32 v32, v64, v32
	v_add_f32_e32 v64, v65, v33
	v_sub_f32_e32 v33, v65, v33
	v_add_f32_e32 v65, v66, v34
	v_sub_f32_e32 v34, v66, v34
	v_add_f32_e32 v66, v67, v35
	v_sub_f32_e32 v35, v67, v35
	v_add_f32_e32 v67, v68, v36
	v_sub_f32_e32 v36, v68, v36
	v_add_f32_e32 v68, v69, v37
	v_sub_f32_e32 v37, v69, v37
	v_add_f32_e32 v69, v70, v38
	v_sub_f32_e32 v38, v70, v38
	v_add_f32_e32 v70, v71, v39
	v_sub_f32_e32 v39, v71, v39
	v_add_f32_e32 v71, v72, v40
	v_sub_f32_e32 v40, v72, v40
	v_add_f32_e32 v72, v73, v41
	v_sub_f32_e32 v41, v73, v41
	v_add_f32_e32 v73, v74, v42
	v_sub_f32_e32 v42, v74, v42
	v_add_f32_e32 v74, v75, v43
	v_sub_f32_e32 v43, v75, v43
	v_add_f32_e32 v75, v76, v44
	v_sub_f32_e32 v44, v76, v44
	v_add_f32_e32 v76, v77, v45
	v_sub_f32_e32 v45, v77, v45
	v_add_f32_e32 v77, v46, v14
	v_sub_f32_e32 v14, v46, v14
	v_add_f32_e32 v46, v47, v15
	v_sub_f32_e32 v15, v47, v15
	v_add_f32_e32 v47, v48, v16
	v_sub_f32_e32 v16, v48, v16
	v_add_f32_e32 v48, v49, v17
	v_sub_f32_e32 v17, v49, v17
	v_add_f32_e32 v49, v50, v18
	v_sub_f32_e32 v18, v50, v18
	v_add_f32_e32 v50, v51, v19
	v_sub_f32_e32 v19, v51, v19
	v_add_f32_e32 v51, v52, v20
	v_sub_f32_e32 v20, v52, v20
	v_add_f32_e32 v52, v53, v21
	v_sub_f32_e32 v21, v53, v21
	v_add_f32_e32 v53, v54, v22
	v_sub_f32_e32 v22, v54, v22
	v_add_f32_e32 v54, v55, v23
	v_sub_f32_e32 v23, v55, v23
	v_add_f32_e32 v55, v56, v24
	v_sub_f32_e32 v24, v56, v24
	v_add_f32_e32 v56, v57, v25
	v_sub_f32_e32 v25, v57, v25
	v_add_f32_e32 v57, v58, v26
	v_sub_f32_e32 v26, v58, v26
	v_add_f32_e32 v58, v59, v27
	v_sub_f32_e32 v27, v59, v27
	v_add_f32_e32 v59, v60, v28
	v_sub_f32_e32 v28, v60, v28
	v_add_f32_e32 v60, v61, v29
	v_sub_f32_e32 v29, v61, v29
	v_add_f32_e32 v61, v78, v62
	v_sub_f32_e32 v62, v78, v62
	v_add_f32_e32 v78, v30, v31
	v_sub_f32_e32 v30, v30, v31
	v_add_f32_e32 v31, v63, v64
	v_sub_f32_e32 v63, v63, v64
	v_add_f32_e32 v64, v32, v33
	v_sub_f32_e32 v32, v32, v33
	v_add_f32_e32 v33, v65, v66
	v_sub_f32_e32 v65, v65, v66
	v_add_f32_e32 v66, v34, v35
	v_sub_f32_e32 v34, v34, v35
	v_add_f32_e32 v35, v67, v68
	v_sub_f32_e32 v67, v67, v68
	v_add_f32_e32 v68, v36, v37
	v_sub_f32_e32 v36, v36, v37
	v_add_f32_e32 v37, v69, v70
	v_sub_f32_e32 v69, v69, v70
	v_add_f32_e32 v70, v38, v39
	v_sub_f32_e32 v38, v38, v39
	v_add_f32_e32 v39, v71, v72
	v_sub_f32_e32 v71, v71, v72
	v_add_f32_e32 v72, v40, v41
	v_sub_f32_e32 v40, v40, v41
	v_add_f32_e32 v41, v73, v74
	v_sub_f32_e32 v73, v73, v74
	v_add_f32_e32 v74, v42, v43
	v_sub_f32_e32 v42, v42, v43
	v_add_f32_e32 v43, v75, v76
	v_sub_f32_e32 v75, v75, v76
	v_add_f32_e32 v76, v44, v45
	v_sub_f32_e32 v44, v44, v45
	v_add_f32_e32 v45, v77, v46
	v_sub_f32_e32 v46, v77, v46
	v_add_f32_e32 v77, v14, v15
	v_sub_f32_e32 v14, v14, v15
	v_add_f32_e32 v15, v47, v48
	v_sub_f32_e32 v47, v47, v48
	v_add_f32_e32 v48, v16, v17
	v_sub_f32_e32 v16, v16, v17
	v_add_f32_e32 v17, v49, v50
	v_sub_f32_e32 v49, v49, v50
	v_add_f32_e32 v50, v18, v19
	v_sub_f32_e32 v18, v18, v19
	v_add_f32_e32 v19, v51, v52
	v_sub_f32_e32 v51, v51, v52
	v_add_f32_e32 v52, v20, v21
	v_sub_f32_e32 v20, v20, v21
	v_add_f32_e32 v21, v53, v54
	v_sub_f32_e32 v53, v53, v54
	v_add_f32_e32 v54, v22, v23
	v_sub_f32_e32 v22, v22, v23
	v_add_f32_e32 v23, v55, v56
	v_sub_f32_e32 v55, v55, v56
	v_add_f32_e32 v56, v24, v25
	v_sub_f32_e32 v24, v24, v25
	v_add_f32_e32 v25, v57, v58
	v_sub_f32_e32 v57, v57, v58
	v_add_f32_e32 v58, v26, v27
	v_sub_f32_e32 v26, v26, v27
	v_add_f32_e32 v27, v59, v60
	v_sub_f32_e32 v59, v59, v60
	v_add_f32_e32 v60, v28, v29
	v_sub_f32_e32 v28, v28, v29
	v_add_f32_e32 v29, v61, v31
	v_sub_f32_e32 v31, v61, v31
	v_add_f32_e32 v61, v78, v64
	v_sub_f32_e32 v64, v78, v64
	v_add_f32_e32 v78, v62, v63
	v_sub_f32_e32 v62, v62, v63
	v_add_f32_e32 v63, v30, v32
	v_sub_f32_e32 v30, v30, v32
	v_add_f32_e32 v32, v33, v35
	v_sub_f32_e32 v33, v33, v35
	v_add_f32_e32 v35, v66, v68
	v_sub_f32_e32 v66, v66, v68
	v_add_f32_e32 v68, v65, v67
	v_sub_f32_e32 v65, v65, v67
	v_add_f32_e32 v67, v34, v36
	v_sub_f32_e32 v34, v34, v36
	v_add_f32_e32 v36, v37, v39
	v_sub_f32_e32 v37, v37, v39
	v_add_f32_e32 v39, v70, v72
	v_sub_f32_e32 v70, v70, v72
	v_add_f32_e32 v72, v69, v71
	v_sub_f32_e32 v69, v69, v71
	v_add_f32_e32 v71, v38, v40
	v_sub_f32_e32 v38, v38, v40
	v_add_f32_e32 v40, v41, v43
	v_sub_f32_e32 v41, v41, v43
	v_add_f32_e32 v43, v74, v76
	v_sub_f32_e32 v74, v74, v76
	v_add_f32_e32 v76, v73, v75
	v_sub_f32_e32 v73, v73, v75
	v_add_f32_e32 v75, v42, v44
	v_sub_f32_e32 v42, v42, v44
	v_add_f32_e32 v44, v45, v15
	v_sub_f32_e32 v15, v45, v15
	v_add_f32_e32 v45, v77, v48
	v_sub_f32_e32 v48, v77, v48
	v_add_f32_e32 v77, v46, v47
	v_sub_f32_e32 v46, v46, v47
	v_add_f32_e32 v47, v14, v16
	v_sub_f32_e32 v14, v14, v16
	v_add_f32_e32 v16, v17, v19
	v_sub_f32_e32 v17, v17, v19
	v_add_f32_e32 v19, v50, v52
	v_sub_f32_e32 v50, v50, v52
	v_add_f32_e32 v52, v49, v51
	v_sub_f32_e32 v49, v49, v51
	v_add_f32_e32 v51, v18, v20
	v_sub_f32_e32 v18, v18, v20
	v_add_f32_e32 v20, v21, v23
	v_sub_f32_e32 v21, v21, v23
	v_add_f32_e32 v23, v54, v56
	v_sub_f32_e32 v54, v54, v56
	v_add_f32_e32 v56, v53, v55
	v_sub_f32_e32 v53, v53, v55
	v_add_f32_e32 v55, v22, v24
	v_sub_f32_e32 v22, v22, v24
	v_add_f32_e32 v24, v25, v27
	v_sub_f32_e32 v25, v25, v27
	v_add_f32_e32 v27, v58, v60
	v_sub_f32_e32 v58, v58, v60
	v_add_f32_e32 v60, v57, v59
	v_sub_f32_e32 v57, v57, v59
	v_add_f32_e32 v59, v26, v28
	v_sub_f32_e32 v26, v26, v28
	v_add_f32_e32 v28, v29, v32
	v_sub_f32_e32 v29, v29, v32
	v_add_f32_e32 v32, v61, v35
	v_sub_f32_e32 v35, v61, v35
	v_add_f32_e32 v61, v78, v68
	v_sub_f32_e32 v68, v78, v68
	v_add_f32_e32 v78, v63, v67
	v_sub_f32_e32 v63, v63, v67
	v_add_f32_e32 v67, v31, v33
	v_sub_f32_e32 v31, v31, v33
	v_add_f32_e32 v33, v64, v66
	v_sub_f32_e32 v64, v64, v66
	v_add_f32_e32 v66, v62, v65
	v_sub_f32_e32 v62, v62, v65
	v_add_f32_e32 v65, v30, v34
	v_sub_f32_e32 v30, v30, v34
	v_add_f32_e32 v34, v36, v40
	v_sub_f32_e32 v36, v36, v40
	v_add_f32_e32 v40, v39, v43
	v_sub_f32_e32 v39, v39, v43
	v_add_f32_e32 v43, v72, v76
	v_sub_f32_e32 v72, v72, v76
	v_add_f32_e32 v76, v71, v75
	v_sub_f32_e32 v71, v71, v75
	v_add_f32_e32 v75, v37, v41
	v_sub_f32_e32 v37, v37, v41
	v_add_f32_e32 v41, v70, v74
	v_sub_f32_e32 v70, v70, v74
	v_add_f32_e32 v74, v69, v73
	v_sub_f32_e32 v69, v69, v73
	v_add_f32_e32 v73, v38, v42
	v_sub_f32_e32 v38, v38, v42
	v_add_f32_e32 v42, v44, v16
	v_sub_f32_e32 v16, v44, v16
	v_add_f32_e32 v44, v45, v19
	v_sub_f32_e32 v19, v45, v19
	v_add_f32_e32 v45, v77, v52
	v_sub_f32_e32 v52, v77, v52
	v_add_f32_e32 v77, v47, v51
	v_sub_f32_e32 v47, v47, v51
	v_add_f32_e32 v51, v15, v17
	v_sub_f32_e32 v15, v15, v17
	v_add_f32_e32 v17, v48, v50
	v_sub_f32_e32 v48, v48, v50
	v_add_f32_e32 v50, v46, v49
	v_sub_f32_e32 v46, v46, v49
	v_add_f32_e32 v49, v14, v18
	v_sub_f32_e32 v14, v14, v18
	v_add_f32_e32 v18, v20, v24
	v_sub_f32_e32 v20, v20, v24
	v_add_f32_e32 v24, v23, v27
	v_sub_f32_e32 v23, v23, v27
	v_add_f32_e32 v27, v56, v60
	v_sub_f32_e32 v56, v56, v60
	v_add_f32_e32 v60, v55, v59
	v_sub_f32_e32 v55, v55, v59
	v_add_f32_e32 v59, v21, v25
	v_sub_f32_e32 v21, v21, v25
	v_add_f32_e32 v25, v54, v58
	v_sub_f32_e32 v54, v54, v58
	v_add_f32_e32 v58, v53, v57
	v_sub_f32_e32 v53, v53, v57
	v_add_f32_e32 v57, v22, v26
	v_sub_f32_e32 v22, v22, v26
	v_add_f32_e32 v26, v28, v34
	v_sub_f32_e32 v28, v28, v34
	v_add_f32_e32 v34, v32, v40
	v_add_f32_e32 v80, v67, v75
	v_sub_f32_e32 v81, v67, v75
	v_add_f32_e32 v67, v33, v41
	v_sub_f32_e32 v82, v33, v41
	v_add_f32_e32 v41, v65, v73
	v_sub_f32_e32 v84, v65, v73
	v_add_f32_e32 v65, v29, v36
	v_sub_f32_e32 v85, v29, v36
	v_add_f32_e32 v29, v35, v39
	v_sub_f32_e32 v86, v35, v39
	v_add_f32_e32 v94, v30, v38
	v_sub_f32_e32 v95, v30, v38
	v_add_f32_e32 v30, v42, v18
	v_add_f32_e32 v35, v44, v24
	v_sub_f32_e32 v79, v32, v40
	v_add_f32_e32 v32, v61, v43
	v_sub_f32_e32 v61, v61, v43
	v_add_f32_e32 v40, v78, v76
	v_sub_f32_e32 v78, v78, v76
	v_add_f32_e32 v33, v66, v74
	v_sub_f32_e32 v83, v66, v74
	v_add_f32_e32 v88, v63, v71
	v_sub_f32_e32 v89, v63, v71
	v_add_f32_e32 v63, v31, v37
	v_sub_f32_e32 v90, v31, v37
	v_sub_f32_e32 v18, v42, v18
	v_add_f32_e32 v37, v45, v27
	v_sub_f32_e32 v96, v45, v27
	v_add_f32_e32 v27, v77, v60
	v_sub_f32_e32 v97, v77, v60
	v_add_f32_e32 v39, v17, v25
	v_sub_f32_e32 v17, v17, v25
	v_add_f32_e32 v25, v50, v58
	v_sub_f32_e32 v50, v50, v58
	v_add_f32_e32 v58, v49, v57
	v_sub_f32_e32 v49, v49, v57
	v_add_f32_e32 v57, v16, v20
	v_sub_f32_e32 v16, v16, v20
	v_add_f32_e32 v20, v19, v23
	v_add_f32_e32 v74, v26, v30
	v_add_f32_e32 v75, v34, v35
	v_add_f32_e32 v38, v51, v59
	v_sub_f32_e32 v42, v26, v30
	v_sub_f32_e32 v43, v34, v35
	v_add_f32_e32 v76, v32, v37
	v_add_f32_e32 v77, v40, v27
	v_add_f32_e32 v71, v67, v39
	v_sub_f32_e32 v39, v67, v39
	v_add_f32_e32 v73, v41, v58
	v_sub_f32_e32 v41, v41, v58
	v_add_f32_e32 v67, v29, v20
	v_sub_f32_e32 v35, v29, v20
	v_add_f32_e32 v58, v28, v18
	v_sub_f32_e32 v26, v28, v18
	v_add_f32_e32 v60, v61, v96
	v_sub_f32_e32 v28, v61, v96
	v_add_f32_e32 v61, v78, v97
	v_sub_f32_e32 v29, v78, v97
	v_max3_f32 v78, |v74|, 0, |v75|
	v_add_f32_e32 v31, v64, v70
	v_sub_f32_e32 v91, v64, v70
	v_add_f32_e32 v70, v80, v38
	v_max3_f32 v78, v78, |v76|, |v77|
	v_add_f32_e32 v36, v68, v72
	v_sub_f32_e32 v87, v68, v72
	v_add_f32_e32 v72, v33, v25
	v_max3_f32 v78, v78, |v70|, |v71|
	v_sub_f32_e32 v19, v19, v23
	v_add_f32_e32 v23, v52, v56
	v_sub_f32_e32 v98, v52, v56
	v_add_f32_e32 v52, v47, v55
	v_add_f32_e32 v66, v65, v57
	v_max3_f32 v78, v78, |v72|, |v73|
	v_add_f32_e32 v92, v62, v69
	v_sub_f32_e32 v93, v62, v69
	v_sub_f32_e32 v47, v47, v55
	v_add_f32_e32 v55, v15, v21
	v_sub_f32_e32 v15, v15, v21
	v_add_f32_e32 v21, v48, v54
	v_add_f32_e32 v68, v36, v23
	v_add_f32_e32 v69, v88, v52
	v_max3_f32 v78, v78, |v66|, |v67|
	v_sub_f32_e32 v48, v48, v54
	v_add_f32_e32 v54, v46, v53
	v_sub_f32_e32 v99, v46, v53
	v_add_f32_e32 v46, v14, v22
	v_add_f32_e32 v62, v63, v55
	v_sub_f32_e32 v30, v63, v55
	v_add_f32_e32 v63, v31, v21
	v_max3_f32 v78, v78, |v68|, |v69|
	v_sub_f32_e32 v24, v44, v24
	v_sub_f32_e32 v34, v65, v57
	v_add_f32_e32 v64, v92, v54
	v_add_f32_e32 v65, v94, v46
	v_max3_f32 v78, v78, |v62|, |v63|
	v_sub_f32_e32 v51, v51, v59
	v_add_f32_e32 v59, v79, v24
	v_max3_f32 v78, v78, |v64|, |v65|
	v_max3_f32 v78, v78, |v58|, |v59|
	v_sub_f32_e32 v44, v32, v37
	v_sub_f32_e32 v32, v92, v54
	v_add_f32_e32 v54, v81, v51
	v_add_f32_e32 v55, v82, v17
	v_max3_f32 v78, v78, |v60|, |v61|
	v_add_f32_e32 v56, v83, v50
	v_add_f32_e32 v57, v84, v49
	v_max3_f32 v78, v78, |v54|, |v55|
	v_sub_f32_e32 v100, v14, v22
	v_sub_f32_e32 v45, v40, v27
	v_sub_f32_e32 v27, v79, v24
	v_sub_f32_e32 v22, v81, v51
	v_sub_f32_e32 v24, v83, v50
	v_add_f32_e32 v50, v85, v16
	v_add_f32_e32 v51, v86, v19
	v_max3_f32 v78, v78, |v56|, |v57|
	v_sub_f32_e32 v37, v88, v52
	v_add_f32_e32 v52, v87, v98
	v_add_f32_e32 v53, v89, v47
	v_max3_f32 v78, v78, |v50|, |v51|
	v_sub_f32_e32 v40, v33, v25
	v_sub_f32_e32 v31, v31, v21
	v_sub_f32_e32 v33, v94, v46
	v_sub_f32_e32 v21, v89, v47
	v_add_f32_e32 v46, v90, v15
	v_add_f32_e32 v47, v91, v48
	v_max3_f32 v78, v78, |v52|, |v53|
	v_sub_f32_e32 v25, v84, v49
	v_sub_f32_e32 v14, v90, v15
	v_sub_f32_e32 v15, v91, v48
	v_add_f32_e32 v48, v93, v99
	v_add_f32_e32 v49, v95, v100
	v_max3_f32 v78, v78, |v46|, |v47|
	v_max3_f32 v78, v78, |v48|, |v49|
	v_max3_f32 v78, v78, |v42|, |v43|
	v_sub_f32_e32 v38, v80, v38
	v_max3_f32 v78, v78, |v44|, |v45|
	v_max3_f32 v78, v78, |v38|, |v39|
	v_max3_f32 v78, v78, |v40|, |v41|
	v_sub_f32_e32 v36, v36, v23
	v_max3_f32 v78, v78, |v34|, |v35|
	v_max3_f32 v78, v78, |v36|, |v37|
	v_max3_f32 v78, v78, |v30|, |v31|
	v_max3_f32 v78, v78, |v32|, |v33|
	v_max3_f32 v78, v78, |v26|, |v27|
	v_sub_f32_e32 v23, v82, v17
	v_max3_f32 v78, v78, |v28|, |v29|
	v_max3_f32 v78, v78, |v22|, |v23|
	v_sub_f32_e32 v18, v85, v16
	v_sub_f32_e32 v19, v86, v19
	v_max3_f32 v78, v78, |v24|, |v25|
	v_sub_f32_e32 v20, v87, v98
	v_max3_f32 v78, v78, |v18|, |v19|
	v_max3_f32 v78, v78, |v20|, |v21|
	v_sub_f32_e32 v16, v93, v99
	v_sub_f32_e32 v17, v95, v100
	v_max3_f32 v78, v78, |v14|, |v15|
	v_max3_f32 v78, v78, |v16|, |v17|
	ds_bpermute_b32 v79, v6, v78
	s_waitcnt lgkmcnt(0)
	v_max_f32_e32 v79, v79, v79
	v_max_f32_e32 v78, v78, v79
	ds_bpermute_b32 v79, v7, v78
	s_waitcnt lgkmcnt(0)
	v_max_f32_e32 v79, v79, v79
	v_max_f32_e32 v78, v78, v79
	ds_bpermute_b32 v79, v8, v78
	s_waitcnt lgkmcnt(0)
	v_max_f32_e32 v79, v79, v79
	v_max_f32_e32 v78, v78, v79
	ds_bpermute_b32 v79, v9, v78
	s_waitcnt lgkmcnt(0)
	v_max_f32_e32 v79, v79, v79
	v_max_f32_e32 v78, v78, v79
	ds_bpermute_b32 v79, v10, v78
	s_waitcnt lgkmcnt(0)
	v_max_f32_e32 v79, v79, v79
	v_max_f32_e32 v78, v78, v79
	ds_bpermute_b32 v79, v11, v78
	s_waitcnt lgkmcnt(0)
	v_max3_f32 v78, v78, v79, s13
	s_and_saveexec_b64 s[8:9], s[2:3]
	s_cbranch_execz .LBB0_349
	s_add_u32 s38, s68, s10
	s_addc_u32 s39, s69, s11
	v_mul_f32_e32 v79, 0x3a810204, v78
	global_store_dword v12, v79, s[38:39]
	s_branch .LBB0_349
.LBB0_352:
	s_waitcnt vmcnt(0)
	s_cmp_gt_i32 s71, 2
	s_cselect_b64 s[0:1], -1, 0
	s_and_b64 s[2:3], s[14:15], s[0:1]
	s_andn2_b64 vcc, exec, s[2:3]
	s_cbranch_vccnz .LBB0_406
	s_waitcnt vmcnt(0)
	s_barrier
	s_mov_b64 s[2:3], exec
	v_readlane_b32 s4, v254, 5
	v_readlane_b32 s5, v254, 6
	s_and_b64 s[4:5], s[2:3], s[4:5]
	s_mov_b64 exec, s[4:5]
	s_cbranch_execz .LBB0_405
	s_add_i32 s4, 0, 0x23e20
	v_mov_b32_e32 v2, s4
	s_waitcnt vmcnt(0) expcnt(0) lgkmcnt(0)
	ds_read_b32 v4, v2
	s_add_i32 s4, 0, 0x23e24
	v_mov_b32_e32 v2, s4
	ds_read_b32 v2, v2
	s_waitcnt lgkmcnt(1)
	v_cmp_ne_u32_e32 vcc, 0, v4
	s_cbranch_vccnz .LBB0_369
	v_readlane_b32 s4, v254, 0
	v_readlane_b32 s5, v254, 1
	s_load_dwordx2 s[8:9], s[4:5], 0x4
	s_add_u32 s4, s68, 0x4200
	s_addc_u32 s5, s69, 0
	s_add_u32 s6, s68, 0x4400
	s_addc_u32 s7, s69, 0
	s_waitcnt lgkmcnt(0)
	s_mul_i32 s33, s8, s91
	s_add_u32 s8, s68, 0x4500
	s_mul_i32 s33, s33, s9
	s_addc_u32 s9, s69, 0
	s_add_u32 s10, s68, 0x4600
	s_addc_u32 s11, s69, 0
	s_add_u32 s12, s68, 0x4700
	s_addc_u32 s13, s69, 0
	s_add_u32 s14, s68, 0x4800
	s_addc_u32 s15, s69, 0
	s_add_u32 s24, s68, 0x4900
	s_addc_u32 s25, s69, 0
	s_add_u32 s34, s68, 0x4a00
	s_addc_u32 s35, s69, 0
	s_add_u32 s36, s68, 0x4b00
	s_addc_u32 s37, s69, 0
	s_add_u32 s38, s68, 0x4c00
	s_addc_u32 s39, s69, 0
	s_add_u32 s40, s68, 0x4d00
	s_addc_u32 s41, s69, 0
	s_add_u32 s42, s68, 0x4e00
	s_addc_u32 s43, s69, 0
	s_add_u32 s44, s68, 0x4f00
	s_addc_u32 s45, s69, 0
	s_add_u32 s46, s68, 0x5000
	s_addc_u32 s47, s69, 0
	s_add_u32 s48, s68, 0x5100
	s_addc_u32 s49, s69, 0
	s_add_u32 s50, s68, 0x5200
	s_addc_u32 s51, s69, 0
	s_add_u32 s52, s68, 0x5300
	s_addc_u32 s53, s69, 0
	s_mov_b32 s60, 1
	v_mov_b32_e32 v18, 0
	s_branch .LBB0_357
